# speedup vs baseline: 1.0358x; 1.0090x over previous
.LBB0_3:
	s_add_i32 s3, s2, 0xfffffe00
	s_lshr_b32 s8, s3, 3
	s_mul_i32 s9, s8, 0x2493
	s_lshr_b32 s9, s9, 16
	s_mul_i32 s10, s9, 7
	s_sub_u32 s10, s8, s10
	s_cmp_lt_u32 s10, 4
	s_cbranch_scc1 .Lcvt_work
	s_cmp_lt_u32 s9, 32
	s_cbranch_scc0 .LBB0_2
	s_lshl_b32 s9, s9, 3
	s_and_b32 s11, s3, 7
	s_or_b32 s3, s9, s11
	v_cmp_eq_u32_e32 vcc, 0, v0
	v_mov_b32_e32 v1, 0
	s_cmp_eq_u32 s10, 5
	s_cbranch_scc1 .Lcvt_mb_wo
	s_cmp_eq_u32 s10, 4
	s_cbranch_scc1 .Lcvt_mb_kv
	s_cmp_eq_u32 s3, 0
	s_cbranch_scc0 .LBB0_2
	s_load_dwordx2 s[6:7], s[0:1], 0x28
	v_mov_b32_e32 v2, 0
	s_waitcnt lgkmcnt(0)
	s_add_u32 s6, s6, 0xa000000
	s_addc_u32 s7, s7, 0
	s_and_saveexec_b64 s[8:9], vcc
	s_cbranch_execz .LBB0_2
	global_store_dword v1, v2, s[6:7]
	s_endpgm
.Lcvt_mb_wo:
	s_load_dwordx2 s[4:5], s[0:1], 0x20
	s_load_dwordx2 s[6:7], s[0:1], 0x38
	s_lshl_b32 s8, s3, 17
	s_waitcnt lgkmcnt(0)
	s_add_u32 s6, s6, s8
	s_addc_u32 s7, s7, 0
	v_mov_b32_e32 v2, s4
	v_mov_b32_e32 v3, s5
	s_and_saveexec_b64 s[8:9], vcc
	s_cbranch_execz .LBB0_2
	global_store_dwordx2 v1, v[2:3], s[6:7]
	s_endpgm
.Lcvt_mb_kv:
	s_load_dwordx4 s[4:7], s[0:1], 0x10
	s_load_dwordx2 s[14:15], s[0:1], 0x30
	s_lshl_b32 s11, s3, 3
	s_and_b32 s12, s11, 0xffffff8f
	s_and_b32 s13, s11, 0x10
	s_lshl_b32 s13, s13, 2
	s_or_b32 s12, s12, s13
	s_and_b32 s13, s11, 0x60
	s_lshr_b32 s13, s13, 1
	s_or_b32 s12, s12, s13
	s_sub_u32 s13, s11, 0x400
	s_waitcnt lgkmcnt(0)
	s_cmp_lt_u32 s3, 0x80
	s_cselect_b32 s12, s12, s13
	s_cselect_b32 s4, s4, s6
	s_cselect_b32 s5, s5, s7
	s_lshl_b32 s12, s12, 14
	s_add_u32 s4, s4, s12
	s_addc_u32 s5, s5, 0
	s_lshl_b32 s13, s3, 16
	s_add_u32 s13, s13, 0x2000000
	s_add_u32 s14, s14, s13
	s_addc_u32 s15, s15, 0
	v_mov_b32_e32 v2, s4
	v_mov_b32_e32 v3, s5
	s_and_saveexec_b64 s[8:9], vcc
	s_cbranch_execz .LBB0_2
	global_store_dwordx2 v1, v[2:3], s[14:15]
	s_endpgm
.Lcvt_work:
	s_lshl_b32 s9, s9, 2
	s_add_u32 s9, s9, s10
	s_lshl_b32 s9, s9, 3
	s_and_b32 s10, s3, 7
	s_or_b32 s8, s9, s10
	s_add_u32 s9, s8, 0x1000
	s_cmp_lt_u32 s8, 0x2000
	s_cselect_b32 s8, s8, s9
	s_load_dwordx4 s[4:7], s[0:1], 0x28
	s_mov_b32 s9, 0
	s_lshl_b64 s[8:9], s[8:9], 8
	v_or_b32_e32 v6, s8, v0
	v_mov_b32_e32 v7, s9
	s_mov_b64 s[8:9], 0x1fffff
	v_cmp_lt_u64_e32 vcc, s[8:9], v[6:7]
	s_mov_b64 s[10:11], 0
	s_and_saveexec_b64 s[8:9], vcc
	s_xor_b64 s[8:9], exec, s[8:9]
	s_cbranch_execnz .LBB0_17
	s_andn2_saveexec_b64 s[8:9], s[8:9]
	s_cbranch_execnz .LBB0_32

.LBB2_7:
	s_add_i32 s3, s16, s14
	s_ashr_i32 s14, s3, 31
	s_lshr_b32 s14, s14, 26
	s_add_i32 s14, s3, s14
	s_ashr_i32 s15, s14, 6
	s_lshl_b32 s36, s15, 3
	s_sub_i32 s15, 32, s36
	s_min_i32 s15, s15, 8
	s_abs_i32 s16, s15
	v_cvt_f32_u32_e32 v1, s16
	s_sub_i32 s18, 0, s16
	s_andn2_b32 s14, s14, 63
	s_sub_i32 s14, s3, s14
	v_rcp_iflag_f32_e32 v1, v1
	s_abs_i32 s3, s14
	s_xor_b32 s17, s14, s15
	s_ashr_i32 s17, s17, 31
	v_mul_f32_e32 v1, 0x4f7ffffe, v1
	v_cvt_u32_f32_e32 v1, v1
	v_lshlrev_b32_e32 v2, 4, v0
	v_lshrrev_b32_e32 v3, 3, v0
	v_bfe_u32 v4, v0, 2, 4
	v_readfirstlane_b32 s19, v1
	s_mul_i32 s18, s18, s19
	s_mul_hi_u32 s18, s19, s18
	s_add_i32 s19, s19, s18
	s_mul_hi_u32 s18, s3, s19
	s_mul_i32 s19, s18, s16
	s_sub_i32 s3, s3, s19
	s_add_i32 s20, s18, 1
	s_sub_i32 s19, s3, s16
	s_cmp_ge_u32 s3, s16
	s_cselect_b32 s18, s20, s18
	s_cselect_b32 s3, s19, s3
	s_add_i32 s19, s18, 1
	s_cmp_ge_u32 s3, s16
	s_cselect_b32 s3, s19, s18
	s_xor_b32 s3, s3, s17
	s_sub_i32 s33, s3, s17
	s_mul_i32 s15, s33, s15
	s_lshl_b32 s3, s33, 8
	s_sub_i32 s14, s14, s15
	s_add_i32 s16, s3, 0x1000
	s_add_i32 s36, s36, s14
	s_ashr_i32 s17, s16, 31
	s_lshl_b32 s14, s36, 7
	s_lshl_b64 s[18:19], s[16:17], 13
	s_waitcnt lgkmcnt(0)
	s_add_u32 s44, s4, 0xa000000
	s_addc_u32 s45, s5, 0
	v_readfirstlane_b32 s46, v0
	s_mov_b32 s47, 0
	v_mov_b32_e32 v226, 0
	s_cmp_lt_u32 s46, 64
	s_cbranch_scc0 .Lkv_nopoll
.Lkv_poll:
	global_load_dword v227, v226, s[44:45] sc1
	s_waitcnt vmcnt(0)
	v_readfirstlane_b32 s46, v227
	s_cmp_ge_u32 s46, 0x100
	s_cbranch_scc1 .Lkv_nopoll
	s_add_i32 s47, s47, 1
	s_cmp_lt_u32 s47, 0x190
	s_cbranch_scc0 .Lkv_nopoll
	s_sleep 16
	s_branch .Lkv_poll
.Lkv_nopoll:
	s_barrier
	s_add_u32 s18, s6, s18
	v_and_b32_e32 v1, 32, v0
	s_addc_u32 s19, s7, s19
	s_add_i32 s26, 0, 0x10000
	v_and_or_b32 v5, v3, 48, v4
	v_bitop3_b32 v1, v2, v1, 48 bitop3:0x6c
	v_or_b32_e32 v3, 64, v3
	s_movk_i32 s15, 0x70
	v_add_u32_e32 v134, s26, v2
	v_and_or_b32 v1, v0, 64, v1
	v_and_or_b32 v3, v3, s15, v4
	v_readfirstlane_b32 s15, v134
	v_add_u32_e32 v135, 0x2000, v134
	v_lshl_or_b32 v130, v5, 13, v1
	s_mov_b32 m0, s15
	v_readfirstlane_b32 s15, v135
	global_load_lds_dwordx4 v130, s[18:19]
	s_mov_b32 m0, s15
	s_ashr_i32 s15, s14, 31
	s_lshl_b64 s[20:21], s[14:15], 13
	s_add_u32 s20, s4, s20
	s_addc_u32 s21, s5, s21
	s_add_i32 s22, s3, 0x1080
	s_ashr_i32 s23, s22, 31
	s_lshl_b64 s[22:23], s[22:23], 13
	v_add_u32_e32 v136, 0, v2
	s_add_u32 s22, s6, s22
	v_lshl_or_b32 v132, v3, 13, v1
	v_readfirstlane_b32 s17, v136
	v_add_u32_e32 v137, 0x2000, v136
	s_addc_u32 s23, s7, s23
	s_add_i32 s27, 0, 0x14000
	global_load_lds_dwordx4 v132, s[18:19]
	s_mov_b32 m0, s17
	v_readfirstlane_b32 s17, v137
	v_add_u32_e32 v138, s27, v2
	global_load_lds_dwordx4 v130, s[20:21]
	s_mov_b32 m0, s17
	v_readfirstlane_b32 s17, v138
	v_add_u32_e32 v139, 0x2000, v138
	global_load_lds_dwordx4 v132, s[20:21]
	s_mov_b32 m0, s17
	v_readfirstlane_b32 s17, v139
	v_add_u32_e32 v140, 0x4000, v136
	global_load_lds_dwordx4 v130, s[22:23]
	s_mov_b32 m0, s17
	s_add_u32 s24, s20, 0x80
	v_readfirstlane_b32 s17, v140
	v_add_u32_e32 v141, 0x6000, v136
	global_load_lds_dwordx4 v132, s[22:23]
	s_addc_u32 s25, s21, 0
	s_mov_b32 m0, s17
	v_readfirstlane_b32 s17, v141
	global_load_lds_dwordx4 v130, s[24:25]
	s_mov_b32 m0, s17
	s_load_dwordx2 s[0:1], s[0:1], 0x20
	global_load_lds_dwordx4 v132, s[24:25]
	s_add_u32 s24, s18, 0x80
	s_addc_u32 s25, s19, 0
	s_add_i32 s28, 0, 0x18000
	v_add_u32_e32 v143, s28, v2
	v_add_u32_e32 v144, 0x2000, v143
	v_readfirstlane_b32 s17, v143
	s_mov_b32 m0, s17
	v_readfirstlane_b32 s17, v144
	global_load_lds_dwordx4 v130, s[24:25]
	s_mov_b32 m0, s17
	v_lshrrev_b32_e32 v3, 8, v0
	global_load_lds_dwordx4 v132, s[24:25]
	s_mov_b32 s17, 0
	v_mov_b32_e32 v131, 0
	v_cmp_eq_u32_e32 vcc, 1, v3
	s_and_saveexec_b64 s[24:25], vcc
	s_cbranch_execz .LBB2_9
	s_barrier

.LBB2_56:
	s_lshl_b32 s0, s2, 5
	s_lshr_b32 s1, s2, 3
	s_and_b32 s0, s0, 0x60
	s_lshl_b32 s3, s2, 1
	s_or_b32 s0, s0, s1
	v_lshrrev_b32_e32 v3, 3, v0
	v_bfe_u32 v4, v0, 2, 4
	s_and_b32 s20, s3, 8
	s_bfe_u32 s3, s2, 0x30003
	s_lshr_b32 s21, s0, 3
	v_and_or_b32 v5, v3, 48, v4
	v_or_b32_e32 v3, 64, v3
	s_movk_i32 s0, 0x70
	s_or_b32 s22, s20, s3
	v_and_or_b32 v3, v3, s0, v4
	s_lshl_b32 s0, s21, 21
	s_waitcnt lgkmcnt(0)
	s_lshl_b32 s46, s2, 16
	s_add_u32 s46, s46, 0x2000000
	s_add_u32 s44, s6, s46
	s_addc_u32 s45, s7, 0
	s_load_dwordx2 s[46:47], s[44:45], 0x0
	s_add_u32 s54, s4, 0xa000000
	s_addc_u32 s55, s5, 0
	s_mov_b32 s48, 0
	s_mov_b32 s50, 0
	s_mov_b32 s51, 0
	v_cmp_eq_u32_e64 s[56:57], 0, v0
	v_lshlrev_b32_e32 v226, 5, v0
	v_lshlrev_b32_e32 v227, 4, v0
	s_add_u32 s0, s6, s0
	v_lshlrev_b32_e32 v1, 4, v0
	v_and_b32_e32 v2, 32, v0
	s_addc_u32 s1, s7, 0
	s_add_i32 s23, 0, 0x10000
	v_bitop3_b32 v2, v1, v2, 48 bitop3:0x6c
	v_add_u32_e32 v141, s23, v1
	v_and_or_b32 v2, v0, 64, v2
	v_readfirstlane_b32 s6, v141
	v_add_u32_e32 v142, 0x2000, v141
	v_lshl_or_b32 v132, v5, 13, v2
	s_mov_b32 m0, s6
	v_readfirstlane_b32 s6, v142
	global_load_lds_dwordx4 v132, s[0:1]
	s_mov_b32 m0, s6
	s_lshl_b32 s6, s22, 21
	s_add_u32 s6, s4, s6
	s_addc_u32 s7, s5, 0
	v_add_u32_e32 v140, 0, v1
	s_add_u32 s16, s0, 0x100000
	v_lshl_or_b32 v130, v3, 13, v2
	v_readfirstlane_b32 s14, v140
	v_add_u32_e32 v144, 0x2000, v140
	s_addc_u32 s17, s1, 0
	s_add_i32 s24, 0, 0x14000
	global_load_lds_dwordx4 v130, s[0:1]
	s_mov_b32 m0, s14
	v_readfirstlane_b32 s14, v144
	v_add_u32_e32 v145, s24, v1
	global_load_lds_dwordx4 v132, s[6:7]
	s_mov_b32 m0, s14
	v_readfirstlane_b32 s14, v145
	v_add_u32_e32 v146, 0x2000, v145
	global_load_lds_dwordx4 v130, s[6:7]
	s_mov_b32 m0, s14
	v_readfirstlane_b32 s14, v146
	v_add_u32_e32 v148, 0x4000, v140
	global_load_lds_dwordx4 v132, s[16:17]
	s_mov_b32 m0, s14
	s_add_u32 s14, s6, 0x100000
	v_readfirstlane_b32 s18, v148
	v_add_u32_e32 v149, 0x6000, v140
	global_load_lds_dwordx4 v130, s[16:17]
	s_addc_u32 s15, s7, 0
	s_mov_b32 m0, s18
	v_readfirstlane_b32 s18, v149
	global_load_lds_dwordx4 v132, s[14:15]
	s_mov_b32 m0, s18
	v_lshrrev_b32_e32 v2, 8, v0
	global_load_lds_dwordx4 v130, s[14:15]
	v_mov_b32_e32 v133, 0
	v_mov_b32_e32 v131, v133
	v_cmp_eq_u32_e32 vcc, 1, v2
	s_and_saveexec_b64 s[18:19], vcc
	s_cbranch_execz .LBB2_58
	s_barrier

.LBB2_59:
	ds_read_b128 v[160:163], v157
	ds_read_b128 v[164:167], v157 offset:1024
	ds_read_b128 v[168:171], v157 offset:2048
	ds_read_b128 v[172:175], v157 offset:3072
	s_add_u32 s24, s4, s2
	s_addc_u32 s25, s5, s3
	s_add_u32 s24, s24, 0x80
	s_addc_u32 s25, s25, 0
	v_readfirstlane_b32 s26, v158
	v_lshl_add_u64 v[176:177], s[24:25], 0, v[132:133]
	s_mov_b32 m0, s26
	s_nop 0
	global_load_lds_dwordx4 v[176:177], off
	v_lshl_add_u64 v[176:177], s[24:25], 0, v[130:131]
	v_readfirstlane_b32 s24, v159
	s_mov_b32 m0, s24
	s_nop 0
	global_load_lds_dwordx4 v[176:177], off
	ds_read_b128 v[176:179], v138
	ds_read_b128 v[180:183], v138 offset:1024
	ds_read_b128 v[184:187], v137
	ds_read_b128 v[188:191], v137 offset:1024
	ds_read_b128 v[192:195], v136
	ds_read_b128 v[196:199], v136 offset:1024
	ds_read_b128 v[200:203], v135
	ds_read_b128 v[204:207], v135 offset:1024
	s_waitcnt lgkmcnt(8)
	s_barrier
	s_waitcnt lgkmcnt(0)
	s_setprio 1
	s_waitcnt lgkmcnt(0)
	v_mfma_f32_16x16x32_f16 v[126:129], v[160:163], v[176:179], v[126:129]
	v_mfma_f32_16x16x32_f16 v[122:125], v[168:171], v[176:179], v[122:125]
	v_mfma_f32_16x16x32_f16 v[118:121], v[160:163], v[184:187], v[118:121]
	v_mfma_f32_16x16x32_f16 v[114:117], v[168:171], v[184:187], v[114:117]
	v_mfma_f32_16x16x32_f16 v[110:113], v[160:163], v[192:195], v[110:113]
	v_mfma_f32_16x16x32_f16 v[106:109], v[168:171], v[192:195], v[106:109]
	v_mfma_f32_16x16x32_f16 v[102:105], v[160:163], v[200:203], v[102:105]
	v_mfma_f32_16x16x32_f16 v[98:101], v[168:171], v[200:203], v[98:101]
	v_mfma_f32_16x16x32_f16 v[126:129], v[164:167], v[180:183], v[126:129]
	v_mfma_f32_16x16x32_f16 v[122:125], v[172:175], v[180:183], v[122:125]
	v_mfma_f32_16x16x32_f16 v[118:121], v[164:167], v[188:191], v[118:121]
	v_mfma_f32_16x16x32_f16 v[114:117], v[172:175], v[188:191], v[114:117]
	v_mfma_f32_16x16x32_f16 v[110:113], v[164:167], v[196:199], v[110:113]
	v_mfma_f32_16x16x32_f16 v[106:109], v[172:175], v[196:199], v[106:109]
	v_mfma_f32_16x16x32_f16 v[102:105], v[164:167], v[204:207], v[102:105]
	v_mfma_f32_16x16x32_f16 v[98:101], v[172:175], v[204:207], v[98:101]
	s_setprio 0
	s_barrier
	s_add_u32 s26, s0, s2
	s_addc_u32 s27, s1, s3
	s_add_u32 s24, s26, 0x100
	s_addc_u32 s25, s27, 0
	v_readfirstlane_b32 s28, v141
	v_lshl_add_u64 v[224:225], s[24:25], 0, v[132:133]
	s_mov_b32 m0, s28
	ds_read_b128 v[208:211], v153
	ds_read_b128 v[212:215], v153 offset:1024
	ds_read_b128 v[216:219], v153 offset:2048
	ds_read_b128 v[220:223], v153 offset:3072
	global_load_lds_dwordx4 v[224:225], off
	v_lshl_add_u64 v[224:225], s[24:25], 0, v[130:131]
	v_readfirstlane_b32 s24, v142
	s_mov_b32 m0, s24
	s_nop 0
	global_load_lds_dwordx4 v[224:225], off
	s_barrier
	s_waitcnt lgkmcnt(0)
	s_setprio 1
	s_waitcnt lgkmcnt(0)
	v_mfma_f32_16x16x32_f16 v[94:97], v[208:211], v[176:179], v[94:97]
	v_mfma_f32_16x16x32_f16 v[90:93], v[216:219], v[176:179], v[90:93]
	v_mfma_f32_16x16x32_f16 v[86:89], v[208:211], v[184:187], v[86:89]
	v_mfma_f32_16x16x32_f16 v[82:85], v[216:219], v[184:187], v[82:85]
	v_mfma_f32_16x16x32_f16 v[78:81], v[208:211], v[192:195], v[78:81]
	v_mfma_f32_16x16x32_f16 v[74:77], v[216:219], v[192:195], v[74:77]
	v_mfma_f32_16x16x32_f16 v[70:73], v[208:211], v[200:203], v[70:73]
	v_mfma_f32_16x16x32_f16 v[66:69], v[216:219], v[200:203], v[66:69]
	v_mfma_f32_16x16x32_f16 v[94:97], v[212:215], v[180:183], v[94:97]
	v_mfma_f32_16x16x32_f16 v[90:93], v[220:223], v[180:183], v[90:93]
	v_mfma_f32_16x16x32_f16 v[86:89], v[212:215], v[188:191], v[86:89]
	v_mfma_f32_16x16x32_f16 v[82:85], v[220:223], v[188:191], v[82:85]
	v_mfma_f32_16x16x32_f16 v[78:81], v[212:215], v[196:199], v[78:81]
	v_mfma_f32_16x16x32_f16 v[74:77], v[220:223], v[196:199], v[74:77]
	v_mfma_f32_16x16x32_f16 v[70:73], v[212:215], v[204:207], v[70:73]
	v_mfma_f32_16x16x32_f16 v[66:69], v[220:223], v[204:207], v[66:69]
	s_setprio 0
	s_add_u32 s28, s6, s2
	s_addc_u32 s29, s7, s3
	s_add_u32 s24, s28, 0x100
	s_addc_u32 s25, s29, 0
	v_readfirstlane_b32 s30, v140
	v_lshl_add_u64 v[224:225], s[24:25], 0, v[132:133]
	s_mov_b32 m0, s30
	s_barrier
	ds_read_b128 v[176:179], v138 offset:16384
	ds_read_b128 v[180:183], v138 offset:17408
	ds_read_b128 v[184:187], v137 offset:16384
	ds_read_b128 v[188:191], v137 offset:17408
	ds_read_b128 v[192:195], v136 offset:16384
	ds_read_b128 v[196:199], v136 offset:17408
	ds_read_b128 v[200:203], v135 offset:16384
	ds_read_b128 v[204:207], v135 offset:17408
	global_load_lds_dwordx4 v[224:225], off
	v_lshl_add_u64 v[224:225], s[24:25], 0, v[130:131]
	v_readfirstlane_b32 s24, v144
	s_mov_b32 m0, s24
	s_nop 0
	global_load_lds_dwordx4 v[224:225], off
	s_barrier
	s_waitcnt lgkmcnt(0)
	s_setprio 1
	s_waitcnt lgkmcnt(0)
	v_mfma_f32_16x16x32_f16 v[62:65], v[160:163], v[176:179], v[62:65]
	v_mfma_f32_16x16x32_f16 v[58:61], v[168:171], v[176:179], v[58:61]
	v_mfma_f32_16x16x32_f16 v[54:57], v[160:163], v[184:187], v[54:57]
	v_mfma_f32_16x16x32_f16 v[50:53], v[168:171], v[184:187], v[50:53]
	v_mfma_f32_16x16x32_f16 v[46:49], v[160:163], v[192:195], v[46:49]
	v_mfma_f32_16x16x32_f16 v[42:45], v[168:171], v[192:195], v[42:45]
	v_mfma_f32_16x16x32_f16 v[38:41], v[160:163], v[200:203], v[38:41]
	v_mfma_f32_16x16x32_f16 v[34:37], v[168:171], v[200:203], v[34:37]
	v_mfma_f32_16x16x32_f16 v[62:65], v[164:167], v[180:183], v[62:65]
	v_mfma_f32_16x16x32_f16 v[58:61], v[172:175], v[180:183], v[58:61]
	v_mfma_f32_16x16x32_f16 v[54:57], v[164:167], v[188:191], v[54:57]
	v_mfma_f32_16x16x32_f16 v[50:53], v[172:175], v[188:191], v[50:53]
	v_mfma_f32_16x16x32_f16 v[46:49], v[164:167], v[196:199], v[46:49]
	v_mfma_f32_16x16x32_f16 v[42:45], v[172:175], v[196:199], v[42:45]
	v_mfma_f32_16x16x32_f16 v[38:41], v[164:167], v[204:207], v[38:41]
	v_mfma_f32_16x16x32_f16 v[34:37], v[172:175], v[204:207], v[34:37]
	s_setprio 0
	s_barrier
	s_add_u32 s30, s16, s2
	s_addc_u32 s31, s17, s3
	s_add_u32 s24, s30, 0x100
	s_addc_u32 s25, s31, 0
	v_readfirstlane_b32 s33, v145
	v_lshl_add_u64 v[160:161], s[24:25], 0, v[132:133]
	s_mov_b32 m0, s33
	s_nop 0
	global_load_lds_dwordx4 v[160:161], off
	v_lshl_add_u64 v[160:161], s[24:25], 0, v[130:131]
	v_readfirstlane_b32 s24, v146
	s_mov_b32 m0, s24
	s_nop 0
	global_load_lds_dwordx4 v[160:161], off
	s_and_b32 s49, s48, 3
	s_add_i32 s48, s48, 1
	s_cmp_eq_u32 s49, 0
	s_cbranch_scc1 .Lkv_issue
	s_cmp_eq_u32 s49, 2
	s_cbranch_scc1 .Lkv_conv
.Lkv_plain:
	s_waitcnt vmcnt(6)
	s_branch .Lkv_join
.Lkv_issue:
	s_cmp_lt_u32 s50, 8
	s_cbranch_scc0 .Lkv_plain
	s_lshl_b32 s49, s50, 14
	s_add_u32 s52, s46, s49
	s_addc_u32 s53, s47, 0
	global_load_dwordx4 v[228:231], v226, s[52:53] nt
	global_load_dwordx4 v[232:235], v226, s[52:53] offset:16 nt
	s_add_i32 s50, s50, 1
	s_waitcnt vmcnt(8)
	s_branch .Lkv_join
.Lkv_conv:
	s_cmp_lt_u32 s51, s50
	s_cbranch_scc0 .Lkv_plain
	v_cvt_pk_f16_f32 v228, v228, v229
	v_cvt_pk_f16_f32 v229, v230, v231
	v_cvt_pk_f16_f32 v230, v232, v233
	v_cvt_pk_f16_f32 v231, v234, v235
	s_lshl_b32 s49, s51, 13
	s_add_u32 s52, s44, s49
	s_addc_u32 s53, s45, 0
	global_store_dwordx4 v227, v[228:231], s[52:53] sc1
	s_add_i32 s51, s51, 1
	s_waitcnt vmcnt(7)
.Lkv_join:
	s_barrier
	s_setprio 1
	v_mfma_f32_16x16x32_f16 v[30:33], v[208:211], v[176:179], v[30:33]
	v_mfma_f32_16x16x32_f16 v[26:29], v[216:219], v[176:179], v[26:29]
	v_mfma_f32_16x16x32_f16 v[22:25], v[208:211], v[184:187], v[22:25]
	v_mfma_f32_16x16x32_f16 v[18:21], v[216:219], v[184:187], v[18:21]
	v_mfma_f32_16x16x32_f16 v[14:17], v[208:211], v[192:195], v[14:17]
	v_mfma_f32_16x16x32_f16 v[10:13], v[216:219], v[192:195], v[10:13]
	v_mfma_f32_16x16x32_f16 v[6:9], v[208:211], v[200:203], v[6:9]
	v_mfma_f32_16x16x32_f16 v[2:5], v[216:219], v[200:203], v[2:5]
	v_mfma_f32_16x16x32_f16 v[30:33], v[212:215], v[180:183], v[30:33]
	v_mfma_f32_16x16x32_f16 v[26:29], v[220:223], v[180:183], v[26:29]
	v_mfma_f32_16x16x32_f16 v[22:25], v[212:215], v[188:191], v[22:25]
	v_mfma_f32_16x16x32_f16 v[18:21], v[220:223], v[188:191], v[18:21]
	v_mfma_f32_16x16x32_f16 v[14:17], v[212:215], v[196:199], v[14:17]
	v_mfma_f32_16x16x32_f16 v[10:13], v[220:223], v[196:199], v[10:13]
	v_mfma_f32_16x16x32_f16 v[6:9], v[212:215], v[204:207], v[6:9]
	v_mfma_f32_16x16x32_f16 v[2:5], v[220:223], v[204:207], v[2:5]
	s_setprio 0
	s_barrier
	ds_read_b128 v[160:163], v143
	ds_read_b128 v[164:167], v143 offset:1024
	ds_read_b128 v[168:171], v143 offset:2048
	ds_read_b128 v[172:175], v143 offset:3072
	s_add_u32 s24, s18, s2
	s_addc_u32 s25, s19, s3
	v_readfirstlane_b32 s33, v148
	v_lshl_add_u64 v[208:209], s[24:25], 0, v[132:133]
	s_mov_b32 m0, s33
	ds_read_b128 v[176:179], v138 offset:32768
	ds_read_b128 v[180:183], v138 offset:33792
	ds_read_b128 v[184:187], v137 offset:32768
	ds_read_b128 v[188:191], v137 offset:33792
	ds_read_b128 v[192:195], v136 offset:32768
	ds_read_b128 v[196:199], v136 offset:33792
	ds_read_b128 v[200:203], v135 offset:32768
	ds_read_b128 v[204:207], v135 offset:33792
	global_load_lds_dwordx4 v[208:209], off
	v_lshl_add_u64 v[208:209], s[24:25], 0, v[130:131]
	v_readfirstlane_b32 s24, v149
	s_mov_b32 m0, s24
	s_nop 0
	global_load_lds_dwordx4 v[208:209], off
	s_waitcnt lgkmcnt(8)
	s_barrier
	s_waitcnt lgkmcnt(0)
	s_setprio 1
	s_waitcnt lgkmcnt(0)
	v_mfma_f32_16x16x32_f16 v[126:129], v[160:163], v[176:179], v[126:129]
	v_mfma_f32_16x16x32_f16 v[122:125], v[168:171], v[176:179], v[122:125]
	v_mfma_f32_16x16x32_f16 v[118:121], v[160:163], v[184:187], v[118:121]
	v_mfma_f32_16x16x32_f16 v[114:117], v[168:171], v[184:187], v[114:117]
	v_mfma_f32_16x16x32_f16 v[110:113], v[160:163], v[192:195], v[110:113]
	v_mfma_f32_16x16x32_f16 v[106:109], v[168:171], v[192:195], v[106:109]
	v_mfma_f32_16x16x32_f16 v[102:105], v[160:163], v[200:203], v[102:105]
	v_mfma_f32_16x16x32_f16 v[98:101], v[168:171], v[200:203], v[98:101]
	v_mfma_f32_16x16x32_f16 v[126:129], v[164:167], v[180:183], v[126:129]
	v_mfma_f32_16x16x32_f16 v[122:125], v[172:175], v[180:183], v[122:125]
	v_mfma_f32_16x16x32_f16 v[118:121], v[164:167], v[188:191], v[118:121]
	v_mfma_f32_16x16x32_f16 v[114:117], v[172:175], v[188:191], v[114:117]
	v_mfma_f32_16x16x32_f16 v[110:113], v[164:167], v[196:199], v[110:113]
	v_mfma_f32_16x16x32_f16 v[106:109], v[172:175], v[196:199], v[106:109]
	v_mfma_f32_16x16x32_f16 v[102:105], v[164:167], v[204:207], v[102:105]
	v_mfma_f32_16x16x32_f16 v[98:101], v[172:175], v[204:207], v[98:101]
	s_setprio 0
	s_barrier
	s_add_u32 s24, s26, 0x180
	s_addc_u32 s25, s27, 0
	v_readfirstlane_b32 s26, v150
	v_lshl_add_u64 v[224:225], s[24:25], 0, v[132:133]
	s_mov_b32 m0, s26
	ds_read_b128 v[208:211], v139
	ds_read_b128 v[212:215], v139 offset:1024
	ds_read_b128 v[216:219], v139 offset:2048
	ds_read_b128 v[220:223], v139 offset:3072
	global_load_lds_dwordx4 v[224:225], off
	v_lshl_add_u64 v[224:225], s[24:25], 0, v[130:131]
	v_readfirstlane_b32 s24, v151
	s_mov_b32 m0, s24
	s_nop 0
	global_load_lds_dwordx4 v[224:225], off
	s_barrier
	s_waitcnt lgkmcnt(0)
	s_setprio 1
	s_waitcnt lgkmcnt(0)
	v_mfma_f32_16x16x32_f16 v[94:97], v[208:211], v[176:179], v[94:97]
	v_mfma_f32_16x16x32_f16 v[90:93], v[216:219], v[176:179], v[90:93]
	v_mfma_f32_16x16x32_f16 v[86:89], v[208:211], v[184:187], v[86:89]
	v_mfma_f32_16x16x32_f16 v[82:85], v[216:219], v[184:187], v[82:85]
	v_mfma_f32_16x16x32_f16 v[78:81], v[208:211], v[192:195], v[78:81]
	v_mfma_f32_16x16x32_f16 v[74:77], v[216:219], v[192:195], v[74:77]
	v_mfma_f32_16x16x32_f16 v[70:73], v[208:211], v[200:203], v[70:73]
	v_mfma_f32_16x16x32_f16 v[66:69], v[216:219], v[200:203], v[66:69]
	v_mfma_f32_16x16x32_f16 v[94:97], v[212:215], v[180:183], v[94:97]
	v_mfma_f32_16x16x32_f16 v[90:93], v[220:223], v[180:183], v[90:93]
	v_mfma_f32_16x16x32_f16 v[86:89], v[212:215], v[188:191], v[86:89]
	v_mfma_f32_16x16x32_f16 v[82:85], v[220:223], v[188:191], v[82:85]
	v_mfma_f32_16x16x32_f16 v[78:81], v[212:215], v[196:199], v[78:81]
	v_mfma_f32_16x16x32_f16 v[74:77], v[220:223], v[196:199], v[74:77]
	v_mfma_f32_16x16x32_f16 v[70:73], v[212:215], v[204:207], v[70:73]
	v_mfma_f32_16x16x32_f16 v[66:69], v[220:223], v[204:207], v[66:69]
	s_setprio 0
	s_add_u32 s24, s28, 0x180
	s_addc_u32 s25, s29, 0
	v_readfirstlane_b32 s26, v152
	v_lshl_add_u64 v[224:225], s[24:25], 0, v[132:133]
	s_mov_b32 m0, s26
	s_barrier
	ds_read_b128 v[176:179], v138 offset:49152
	ds_read_b128 v[180:183], v138 offset:50176
	ds_read_b128 v[184:187], v137 offset:49152
	ds_read_b128 v[188:191], v137 offset:50176
	ds_read_b128 v[192:195], v136 offset:49152
	ds_read_b128 v[196:199], v136 offset:50176
	ds_read_b128 v[200:203], v135 offset:49152
	ds_read_b128 v[204:207], v135 offset:50176
	global_load_lds_dwordx4 v[224:225], off
	v_lshl_add_u64 v[224:225], s[24:25], 0, v[130:131]
	v_readfirstlane_b32 s24, v154
	s_mov_b32 m0, s24
	s_nop 0
	global_load_lds_dwordx4 v[224:225], off
	s_barrier
	s_waitcnt lgkmcnt(0)
	s_setprio 1
	s_waitcnt lgkmcnt(0)
	v_mfma_f32_16x16x32_f16 v[62:65], v[160:163], v[176:179], v[62:65]
	v_mfma_f32_16x16x32_f16 v[58:61], v[168:171], v[176:179], v[58:61]
	v_mfma_f32_16x16x32_f16 v[54:57], v[160:163], v[184:187], v[54:57]
	v_mfma_f32_16x16x32_f16 v[50:53], v[168:171], v[184:187], v[50:53]
	v_mfma_f32_16x16x32_f16 v[46:49], v[160:163], v[192:195], v[46:49]
	v_mfma_f32_16x16x32_f16 v[42:45], v[168:171], v[192:195], v[42:45]
	v_mfma_f32_16x16x32_f16 v[38:41], v[160:163], v[200:203], v[38:41]
	v_mfma_f32_16x16x32_f16 v[34:37], v[168:171], v[200:203], v[34:37]
	v_mfma_f32_16x16x32_f16 v[62:65], v[164:167], v[180:183], v[62:65]
	v_mfma_f32_16x16x32_f16 v[58:61], v[172:175], v[180:183], v[58:61]
	v_mfma_f32_16x16x32_f16 v[54:57], v[164:167], v[188:191], v[54:57]
	v_mfma_f32_16x16x32_f16 v[50:53], v[172:175], v[188:191], v[50:53]
	v_mfma_f32_16x16x32_f16 v[46:49], v[164:167], v[196:199], v[46:49]
	v_mfma_f32_16x16x32_f16 v[42:45], v[172:175], v[196:199], v[42:45]
	v_mfma_f32_16x16x32_f16 v[38:41], v[164:167], v[204:207], v[38:41]
	v_mfma_f32_16x16x32_f16 v[34:37], v[172:175], v[204:207], v[34:37]
	s_setprio 0
	s_barrier
	s_add_u32 s24, s30, 0x180
	s_addc_u32 s25, s31, 0
	v_readfirstlane_b32 s26, v155
	v_lshl_add_u64 v[160:161], s[24:25], 0, v[132:133]
	s_mov_b32 m0, s26
	s_nop 0
	global_load_lds_dwordx4 v[160:161], off
	v_lshl_add_u64 v[160:161], s[24:25], 0, v[130:131]
	v_readfirstlane_b32 s24, v156
	s_mov_b32 m0, s24
	s_nop 0
	global_load_lds_dwordx4 v[160:161], off
	s_waitcnt vmcnt(6)
	s_barrier
	s_setprio 1
	v_mfma_f32_16x16x32_f16 v[30:33], v[208:211], v[176:179], v[30:33]
	v_mfma_f32_16x16x32_f16 v[26:29], v[216:219], v[176:179], v[26:29]
	v_mfma_f32_16x16x32_f16 v[22:25], v[208:211], v[184:187], v[22:25]
	v_mfma_f32_16x16x32_f16 v[18:21], v[216:219], v[184:187], v[18:21]
	v_mfma_f32_16x16x32_f16 v[14:17], v[208:211], v[192:195], v[14:17]
	v_mfma_f32_16x16x32_f16 v[10:13], v[216:219], v[192:195], v[10:13]
	v_mfma_f32_16x16x32_f16 v[6:9], v[208:211], v[200:203], v[6:9]
	v_mfma_f32_16x16x32_f16 v[2:5], v[216:219], v[200:203], v[2:5]
	v_mfma_f32_16x16x32_f16 v[30:33], v[212:215], v[180:183], v[30:33]
	v_mfma_f32_16x16x32_f16 v[26:29], v[220:223], v[180:183], v[26:29]
	v_mfma_f32_16x16x32_f16 v[22:25], v[212:215], v[188:191], v[22:25]
	v_mfma_f32_16x16x32_f16 v[18:21], v[220:223], v[188:191], v[18:21]
	v_mfma_f32_16x16x32_f16 v[14:17], v[212:215], v[196:199], v[14:17]
	v_mfma_f32_16x16x32_f16 v[10:13], v[220:223], v[196:199], v[10:13]
	v_mfma_f32_16x16x32_f16 v[6:9], v[212:215], v[204:207], v[6:9]
	v_mfma_f32_16x16x32_f16 v[2:5], v[220:223], v[204:207], v[2:5]
	s_setprio 0
	s_add_i32 s23, s23, 2
	s_add_u32 s2, s2, 0x100
	s_addc_u32 s3, s3, 0
	s_cmp_lt_u32 s23, 60
	s_barrier
	s_cbranch_scc1 .LBB2_59
	s_add_u32 s0, s14, 0x1f80
	v_add_u32_e32 v141, 0xc000, v140
	s_addc_u32 s1, s15, 0
	v_readfirstlane_b32 s2, v141
	v_lshl_add_u64 v[132:133], s[0:1], 0, v[132:133]
	s_mov_b32 m0, s2
	ds_read_b128 v[148:151], v157
	ds_read_b128 v[158:161], v157 offset:1024
	ds_read_b128 v[162:165], v157 offset:2048
	ds_read_b128 v[154:157], v157 offset:3072
	global_load_lds_dwordx4 v[132:133], off
	v_add_u32_e32 v132, 0xe000, v140
	v_lshl_add_u64 v[130:131], s[0:1], 0, v[130:131]
	v_readfirstlane_b32 s0, v132
	s_mov_b32 m0, s0
	s_nop 0
	global_load_lds_dwordx4 v[130:131], off
	ds_read_b128 v[130:133], v138
	ds_read_b128 v[166:169], v138 offset:1024
	ds_read_b128 v[170:173], v137
	ds_read_b128 v[174:177], v137 offset:1024
	ds_read_b128 v[178:181], v136
	ds_read_b128 v[182:185], v136 offset:1024
	ds_read_b128 v[186:189], v135
	ds_read_b128 v[190:193], v135 offset:1024
	s_barrier
	s_waitcnt lgkmcnt(0)
	s_setprio 1
	s_waitcnt lgkmcnt(0)
	v_mfma_f32_16x16x32_f16 v[126:129], v[148:151], v[130:133], v[126:129]
	v_mfma_f32_16x16x32_f16 v[122:125], v[162:165], v[130:133], v[122:125]
	v_mfma_f32_16x16x32_f16 v[118:121], v[148:151], v[170:173], v[118:121]
	v_mfma_f32_16x16x32_f16 v[114:117], v[162:165], v[170:173], v[114:117]
	v_mfma_f32_16x16x32_f16 v[110:113], v[148:151], v[178:181], v[110:113]
	v_mfma_f32_16x16x32_f16 v[106:109], v[162:165], v[178:181], v[106:109]
	v_mfma_f32_16x16x32_f16 v[102:105], v[148:151], v[186:189], v[102:105]
	v_mfma_f32_16x16x32_f16 v[126:129], v[158:161], v[166:169], v[126:129]
	v_mfma_f32_16x16x32_f16 v[122:125], v[154:157], v[166:169], v[122:125]
	v_mfma_f32_16x16x32_f16 v[118:121], v[158:161], v[174:177], v[118:121]
	v_mfma_f32_16x16x32_f16 v[114:117], v[154:157], v[174:177], v[114:117]
	v_mfma_f32_16x16x32_f16 v[110:113], v[158:161], v[182:185], v[110:113]
	v_mfma_f32_16x16x32_f16 v[106:109], v[154:157], v[182:185], v[106:109]
	v_mfma_f32_16x16x32_f16 v[102:105], v[158:161], v[190:193], v[102:105]
	v_mfma_f32_16x16x32_f16 v[98:101], v[162:165], v[186:189], v[98:101]
	v_mfma_f32_16x16x32_f16 v[194:197], v[154:157], v[190:193], v[98:101]
	s_setprio 0
	s_barrier
	s_nop 4
	ds_read_b128 v[98:101], v153
	ds_read_b128 v[198:201], v153 offset:1024
	ds_read_b128 v[202:205], v153 offset:2048
	ds_read_b128 v[206:209], v153 offset:3072
	s_barrier
	s_waitcnt lgkmcnt(0)
	s_setprio 1
	s_waitcnt lgkmcnt(0)
	v_mfma_f32_16x16x32_f16 v[82:85], v[202:205], v[170:173], v[82:85]
	v_mfma_f32_16x16x32_f16 v[78:81], v[98:101], v[178:181], v[78:81]
	v_mfma_f32_16x16x32_f16 v[74:77], v[202:205], v[178:181], v[74:77]
	v_mfma_f32_16x16x32_f16 v[70:73], v[98:101], v[186:189], v[70:73]
	v_mfma_f32_16x16x32_f16 v[94:97], v[98:101], v[130:133], v[94:97]
	v_mfma_f32_16x16x32_f16 v[90:93], v[202:205], v[130:133], v[90:93]
	v_mfma_f32_16x16x32_f16 v[86:89], v[98:101], v[170:173], v[86:89]
	v_mfma_f32_16x16x32_f16 v[82:85], v[206:209], v[174:177], v[82:85]
	v_mfma_f32_16x16x32_f16 v[78:81], v[198:201], v[182:185], v[78:81]
	v_mfma_f32_16x16x32_f16 v[74:77], v[206:209], v[182:185], v[74:77]
	v_mfma_f32_16x16x32_f16 v[70:73], v[198:201], v[190:193], v[70:73]
	v_mfma_f32_16x16x32_f16 v[66:69], v[202:205], v[186:189], v[66:69]
	v_mfma_f32_16x16x32_f16 v[210:213], v[198:201], v[166:169], v[94:97]
	v_mfma_f32_16x16x32_f16 v[166:169], v[206:209], v[166:169], v[90:93]
	v_mfma_f32_16x16x32_f16 v[214:217], v[198:201], v[174:177], v[86:89]
	v_mfma_f32_16x16x32_f16 v[66:69], v[206:209], v[190:193], v[66:69]
	s_setprio 0
	s_barrier
	ds_read_b128 v[86:89], v138 offset:16384
	ds_read_b128 v[90:93], v138 offset:17408
	ds_read_b128 v[94:97], v137 offset:16384
	ds_read_b128 v[130:133], v137 offset:17408
	ds_read_b128 v[170:173], v136 offset:16384
	ds_read_b128 v[174:177], v136 offset:17408
	ds_read_b128 v[178:181], v135 offset:16384
	ds_read_b128 v[182:185], v135 offset:17408
	s_waitcnt vmcnt(4)
	s_barrier
	s_waitcnt lgkmcnt(0)
	s_setprio 1
	s_waitcnt lgkmcnt(0)
	v_mfma_f32_16x16x32_f16 v[62:65], v[148:151], v[86:89], v[62:65]
	v_mfma_f32_16x16x32_f16 v[54:57], v[148:151], v[94:97], v[54:57]
	v_mfma_f32_16x16x32_f16 v[46:49], v[148:151], v[170:173], v[46:49]
	v_mfma_f32_16x16x32_f16 v[42:45], v[162:165], v[170:173], v[42:45]
	v_mfma_f32_16x16x32_f16 v[38:41], v[148:151], v[178:181], v[38:41]
	v_mfma_f32_16x16x32_f16 v[34:37], v[162:165], v[178:181], v[34:37]
	v_mfma_f32_16x16x32_f16 v[62:65], v[158:161], v[90:93], v[62:65]
	v_mfma_f32_16x16x32_f16 v[58:61], v[162:165], v[86:89], v[58:61]
	v_mfma_f32_16x16x32_f16 v[54:57], v[158:161], v[130:133], v[54:57]
	v_mfma_f32_16x16x32_f16 v[50:53], v[162:165], v[94:97], v[50:53]
	v_mfma_f32_16x16x32_f16 v[46:49], v[158:161], v[174:177], v[46:49]
	v_mfma_f32_16x16x32_f16 v[42:45], v[154:157], v[174:177], v[42:45]
	v_mfma_f32_16x16x32_f16 v[38:41], v[158:161], v[182:185], v[38:41]
	v_mfma_f32_16x16x32_f16 v[34:37], v[154:157], v[182:185], v[34:37]
	v_mfma_f32_16x16x32_f16 v[186:189], v[154:157], v[90:93], v[58:61]
	v_mfma_f32_16x16x32_f16 v[190:193], v[154:157], v[130:133], v[50:53]
	s_setprio 0
	s_setprio 1
	v_mfma_f32_16x16x32_f16 v[14:17], v[98:101], v[170:173], v[14:17]
	v_mfma_f32_16x16x32_f16 v[6:9], v[98:101], v[178:181], v[6:9]
	v_mfma_f32_16x16x32_f16 v[30:33], v[98:101], v[86:89], v[30:33]
	v_mfma_f32_16x16x32_f16 v[26:29], v[202:205], v[86:89], v[26:29]
	v_mfma_f32_16x16x32_f16 v[22:25], v[98:101], v[94:97], v[22:25]
	v_mfma_f32_16x16x32_f16 v[18:21], v[202:205], v[94:97], v[18:21]
	v_mfma_f32_16x16x32_f16 v[14:17], v[198:201], v[174:177], v[14:17]
	v_mfma_f32_16x16x32_f16 v[10:13], v[202:205], v[170:173], v[10:13]
	v_mfma_f32_16x16x32_f16 v[6:9], v[198:201], v[182:185], v[6:9]
	v_mfma_f32_16x16x32_f16 v[2:5], v[202:205], v[178:181], v[2:5]
	v_mfma_f32_16x16x32_f16 v[148:151], v[198:201], v[90:93], v[30:33]
	v_mfma_f32_16x16x32_f16 v[152:155], v[206:209], v[90:93], v[26:29]
	v_mfma_f32_16x16x32_f16 v[156:159], v[198:201], v[130:133], v[22:25]
	v_mfma_f32_16x16x32_f16 v[160:163], v[206:209], v[130:133], v[18:21]
	v_mfma_f32_16x16x32_f16 v[170:173], v[206:209], v[174:177], v[10:13]
	v_mfma_f32_16x16x32_f16 v[174:177], v[206:209], v[182:185], v[2:5]
	s_setprio 0
	s_barrier
	s_nop 0
	ds_read_b128 v[2:5], v143
	ds_read_b128 v[10:13], v143 offset:1024
	ds_read_b128 v[22:25], v143 offset:2048
	ds_read_b128 v[140:143], v143 offset:3072
	ds_read_b128 v[18:21], v138 offset:32768
	ds_read_b128 v[26:29], v138 offset:33792
	ds_read_b128 v[30:33], v137 offset:32768
	ds_read_b128 v[50:53], v137 offset:33792
	ds_read_b128 v[58:61], v136 offset:32768
	ds_read_b128 v[178:181], v136 offset:33792
	ds_read_b128 v[182:185], v135 offset:32768
	ds_read_b128 v[198:201], v135 offset:33792
	s_waitcnt vmcnt(2)
	s_barrier
	s_waitcnt lgkmcnt(0)
	s_setprio 1
	s_waitcnt lgkmcnt(0)
	v_mfma_f32_16x16x32_f16 v[86:89], v[2:5], v[18:21], v[126:129]
	v_mfma_f32_16x16x32_f16 v[126:129], v[10:13], v[26:29], v[86:89]
	v_mfma_f32_16x16x32_f16 v[86:89], v[22:25], v[18:21], v[122:125]
	v_mfma_f32_16x16x32_f16 v[130:133], v[140:143], v[26:29], v[86:89]
	v_mfma_f32_16x16x32_f16 v[86:89], v[2:5], v[30:33], v[118:121]
	v_mfma_f32_16x16x32_f16 v[118:121], v[10:13], v[50:53], v[86:89]
	v_mfma_f32_16x16x32_f16 v[86:89], v[22:25], v[30:33], v[114:117]
	v_mfma_f32_16x16x32_f16 v[122:125], v[140:143], v[50:53], v[86:89]
	v_mfma_f32_16x16x32_f16 v[86:89], v[2:5], v[58:61], v[110:113]
	v_mfma_f32_16x16x32_f16 v[94:97], v[10:13], v[178:181], v[86:89]
	v_mfma_f32_16x16x32_f16 v[86:89], v[22:25], v[58:61], v[106:109]
	v_mfma_f32_16x16x32_f16 v[98:101], v[140:143], v[178:181], v[86:89]
	v_mfma_f32_16x16x32_f16 v[86:89], v[2:5], v[182:185], v[102:105]
	v_mfma_f32_16x16x32_f16 v[90:93], v[22:25], v[182:185], v[194:197]
	v_mfma_f32_16x16x32_f16 v[86:89], v[10:13], v[198:201], v[86:89]
	v_mfma_f32_16x16x32_f16 v[90:93], v[140:143], v[198:201], v[90:93]
	s_setprio 0
	s_barrier
	ds_read_b128 v[194:197], v139
	ds_read_b128 v[202:205], v139 offset:1024
	ds_read_b128 v[206:209], v139 offset:2048
	ds_read_b128 v[218:221], v139 offset:3072
	s_waitcnt vmcnt(0)
.Lkv_tail:
	s_cmp_lt_u32 s51, s50
	s_cbranch_scc0 .Lkv_tail_issue
	v_cvt_pk_f16_f32 v228, v228, v229
	v_cvt_pk_f16_f32 v229, v230, v231
	v_cvt_pk_f16_f32 v230, v232, v233
	v_cvt_pk_f16_f32 v231, v234, v235
	s_lshl_b32 s49, s51, 13
	s_add_u32 s52, s44, s49
	s_addc_u32 s53, s45, 0
	global_store_dwordx4 v227, v[228:231], s[52:53] sc1
	s_add_i32 s51, s51, 1
.Lkv_tail_issue:
	s_cmp_lt_u32 s50, 8
	s_cbranch_scc0 .Lkv_tail_done
	s_lshl_b32 s49, s50, 14
	s_add_u32 s52, s46, s49
	s_addc_u32 s53, s47, 0
	global_load_dwordx4 v[228:231], v226, s[52:53] nt
	global_load_dwordx4 v[232:235], v226, s[52:53] offset:16 nt
	s_add_i32 s50, s50, 1
	s_waitcnt vmcnt(0)
	s_branch .Lkv_tail
.Lkv_tail_done:
	s_barrier
	s_waitcnt lgkmcnt(0)
	s_setprio 1
	s_waitcnt lgkmcnt(0)
	v_mfma_f32_16x16x32_f16 v[102:105], v[194:197], v[18:21], v[210:213]
	v_mfma_f32_16x16x32_f16 v[18:21], v[206:209], v[18:21], v[166:169]
	v_mfma_f32_16x16x32_f16 v[114:117], v[218:221], v[26:29], v[18:21]
	v_mfma_f32_16x16x32_f16 v[18:21], v[194:197], v[30:33], v[214:217]
	v_mfma_f32_16x16x32_f16 v[110:113], v[202:205], v[26:29], v[102:105]
	v_mfma_f32_16x16x32_f16 v[102:105], v[202:205], v[50:53], v[18:21]
	v_mfma_f32_16x16x32_f16 v[18:21], v[206:209], v[30:33], v[82:85]
	v_mfma_f32_16x16x32_f16 v[106:109], v[218:221], v[50:53], v[18:21]
	v_mfma_f32_16x16x32_f16 v[18:21], v[194:197], v[58:61], v[78:81]
	v_mfma_f32_16x16x32_f16 v[78:81], v[202:205], v[178:181], v[18:21]
	v_mfma_f32_16x16x32_f16 v[18:21], v[206:209], v[58:61], v[74:77]
	v_mfma_f32_16x16x32_f16 v[82:85], v[218:221], v[178:181], v[18:21]
	v_mfma_f32_16x16x32_f16 v[18:21], v[194:197], v[182:185], v[70:73]
	v_mfma_f32_16x16x32_f16 v[70:73], v[202:205], v[198:201], v[18:21]
	v_mfma_f32_16x16x32_f16 v[18:21], v[206:209], v[182:185], v[66:69]
	v_mfma_f32_16x16x32_f16 v[74:77], v[218:221], v[198:201], v[18:21]
	s_setprio 0
	s_barrier
	ds_read_b128 v[66:69], v138 offset:49152
	ds_read_b128 v[164:167], v138 offset:50176
	ds_read_b128 v[178:181], v137 offset:49152
	ds_read_b128 v[182:185], v137 offset:50176
	ds_read_b128 v[198:201], v136 offset:49152
	ds_read_b128 v[136:139], v136 offset:50176
	ds_read_b128 v[210:213], v135 offset:49152
	ds_read_b128 v[214:217], v135 offset:50176
	s_barrier
	s_waitcnt lgkmcnt(0)
	s_setprio 1
	s_waitcnt lgkmcnt(0)
	v_mfma_f32_16x16x32_f16 v[18:21], v[2:5], v[66:69], v[62:65]
	v_mfma_f32_16x16x32_f16 v[58:61], v[10:13], v[164:167], v[18:21]
	v_mfma_f32_16x16x32_f16 v[18:21], v[22:25], v[66:69], v[186:189]
	v_mfma_f32_16x16x32_f16 v[62:65], v[140:143], v[164:167], v[18:21]
	v_mfma_f32_16x16x32_f16 v[18:21], v[2:5], v[178:181], v[54:57]
	v_mfma_f32_16x16x32_f16 v[50:53], v[10:13], v[182:185], v[18:21]
	v_mfma_f32_16x16x32_f16 v[18:21], v[22:25], v[178:181], v[190:193]
	v_mfma_f32_16x16x32_f16 v[54:57], v[140:143], v[182:185], v[18:21]
	v_mfma_f32_16x16x32_f16 v[18:21], v[2:5], v[198:201], v[46:49]
	v_mfma_f32_16x16x32_f16 v[26:29], v[10:13], v[136:139], v[18:21]
	v_mfma_f32_16x16x32_f16 v[18:21], v[22:25], v[198:201], v[42:45]
	v_mfma_f32_16x16x32_f16 v[2:5], v[2:5], v[210:213], v[38:41]
	v_mfma_f32_16x16x32_f16 v[30:33], v[140:143], v[136:139], v[18:21]
	v_mfma_f32_16x16x32_f16 v[18:21], v[10:13], v[214:217], v[2:5]
	v_mfma_f32_16x16x32_f16 v[2:5], v[22:25], v[210:213], v[34:37]
	v_mfma_f32_16x16x32_f16 v[22:25], v[140:143], v[214:217], v[2:5]
	s_setprio 0
	s_setprio 1
	v_mfma_f32_16x16x32_f16 v[2:5], v[194:197], v[66:69], v[148:151]
	v_mfma_f32_16x16x32_f16 v[42:45], v[202:205], v[164:167], v[2:5]
	v_mfma_f32_16x16x32_f16 v[2:5], v[206:209], v[66:69], v[152:155]
	v_mfma_f32_16x16x32_f16 v[46:49], v[218:221], v[164:167], v[2:5]
	v_mfma_f32_16x16x32_f16 v[2:5], v[194:197], v[178:181], v[156:159]
	v_mfma_f32_16x16x32_f16 v[34:37], v[202:205], v[182:185], v[2:5]
	v_mfma_f32_16x16x32_f16 v[2:5], v[206:209], v[178:181], v[160:163]
	v_mfma_f32_16x16x32_f16 v[38:41], v[218:221], v[182:185], v[2:5]
	v_mfma_f32_16x16x32_f16 v[2:5], v[194:197], v[198:201], v[14:17]
	v_mfma_f32_16x16x32_f16 v[10:13], v[202:205], v[136:139], v[2:5]
	v_mfma_f32_16x16x32_f16 v[2:5], v[206:209], v[198:201], v[170:173]
	v_mfma_f32_16x16x32_f16 v[14:17], v[218:221], v[136:139], v[2:5]
	v_mfma_f32_16x16x32_f16 v[2:5], v[194:197], v[210:213], v[6:9]
	v_mfma_f32_16x16x32_f16 v[6:9], v[206:209], v[210:213], v[174:177]
	v_mfma_f32_16x16x32_f16 v[2:5], v[202:205], v[214:217], v[2:5]
	v_mfma_f32_16x16x32_f16 v[6:9], v[218:221], v[214:217], v[6:9]
	s_setprio 0
	s_movk_i32 s0, 0x100
	v_cmp_gt_u32_e32 vcc, s0, v0
	s_barrier
	s_and_saveexec_b64 s[0:1], vcc
	s_cbranch_execz .LBB2_62
	s_barrier

.LBB2_96:
	s_or_b64 exec, exec, s[0:1]
	s_lshl_b32 s3, s22, 8
	s_and_b32 s0, s3, 0x700
	v_and_b32_e32 v0, 31, v0
	v_or3_b32 v137, v0, s0, v1
	s_lshl_b32 s0, s20, 21
	s_lshl_b32 s1, s21, 20
	v_lshlrev_b32_e32 v142, 6, v134
	v_mov_b32_e32 v143, 0
	s_or_b32 s0, s0, s1
	v_lshl_add_u64 v[0:1], s[10:11], 0, v[142:143]
	v_lshlrev_b32_e32 v142, 4, v135
	s_add_u32 s0, s8, s0
	v_lshl_add_u64 v[0:1], v[0:1], 0, v[142:143]
	s_addc_u32 s1, s9, 0
	v_lshlrev_b32_e32 v142, 8, v137
	s_waitcnt vmcnt(0) lgkmcnt(0)
	s_barrier
	global_load_dwordx4 v[66:69], v[0:1], off
	global_load_dwordx4 v[148:151], v[0:1], off offset:256
	v_lshl_add_u64 v[0:1], s[0:1], 0, v[142:143]
	v_lshlrev_b32_e32 v142, 5, v134
	v_lshlrev_b32_e32 v136, 3, v136
	v_lshl_add_u64 v[0:1], v[0:1], 0, v[142:143]
	v_and_b32_e32 v142, 16, v136
	v_lshl_add_u64 v[0:1], v[0:1], 0, v[142:143]
	v_lshlrev_b32_e32 v142, 7, v134
	v_or_b32_e32 v134, s3, v146
	v_lshl_add_u64 v[136:137], s[12:13], 0, v[142:143]
	v_lshlrev_b32_e32 v142, 5, v135
	v_lshlrev_b32_e32 v134, 9, v134
	v_lshl_add_u64 v[144:145], v[136:137], 0, v[142:143]
	v_and_b32_e32 v142, 0xe9e00, v134
	v_lshl_add_u64 v[134:135], v[144:145], 0, v[142:143]
	global_load_dwordx4 v[152:155], v[134:135], off
	global_load_dwordx4 v[156:159], v[134:135], off offset:16
	v_or_b32_e32 v168, 16, v146
	v_or_b32_e32 v134, s3, v168
	v_lshlrev_b32_e32 v134, 9, v134
	v_and_b32_e32 v142, 0xebe00, v134
	v_lshl_add_u64 v[134:135], v[144:145], 0, v[142:143]
	global_load_dwordx4 v[138:141], v[134:135], off
	s_nop 0
	global_load_dwordx4 v[134:137], v[134:135], off offset:16
	v_add_u32_e32 v142, 0, v147
	ds_read_b128 v[160:163], v142
	v_mov_b32_e32 v164, v130
	v_mov_b32_e32 v147, 0x358637bd
	s_mov_b32 s2, 0x800000
	v_mov_b32_e32 v165, v126
	s_waitcnt lgkmcnt(0)
	v_add_f32_e32 v130, v160, v161
	v_add_f32_e32 v130, v162, v130
	v_add_f32_e32 v130, v163, v130
	v_fmamk_f32 v130, v130, 0x3c000000, v147
	v_mov_b32_e32 v126, v131
	v_mul_f32_e32 v131, 0x4b800000, v130
	v_cmp_gt_f32_e32 vcc, s2, v130
	s_mov_b32 s0, 0x80000
	s_nop 0
	v_cndmask_b32_e32 v130, v130, v131, vcc
	v_rsq_f32_e32 v160, v130
	v_mov_b32_e32 v130, v132
	v_mov_b32_e32 v131, v128
	v_mov_b32_e32 v128, v133
	v_mul_f32_e32 v132, 0x45800000, v160
	v_cndmask_b32_e32 v132, v160, v132, vcc
	v_pk_mul_f32 v[160:161], v[164:165], v[132:133] op_sel_hi:[1,0]
	v_pk_mul_f32 v[162:163], v[126:127], v[132:133] op_sel_hi:[1,0]
	v_pk_mul_f32 v[130:131], v[130:131], v[132:133] op_sel_hi:[1,0]
	v_pk_mul_f32 v[132:133], v[128:129], v[132:133] op_sel_hi:[1,0]
	s_waitcnt vmcnt(5)
	v_mov_b32_e32 v129, v66
	s_waitcnt vmcnt(4)
	v_mov_b32_e32 v128, v148
	v_mov_b32_e32 v66, v149
	v_mov_b32_e32 v126, v150
	v_mov_b32_e32 v127, v68
	v_mov_b32_e32 v68, v151
	v_pk_mul_f32 v[148:149], v[128:129], v[160:161]
	v_pk_mul_f32 v[150:151], v[66:67], v[162:163]
	v_pk_mul_f32 v[130:131], v[126:127], v[130:131]
	v_pk_mul_f32 v[132:133], v[68:69], v[132:133]
	s_waitcnt vmcnt(3)
	v_pk_mul_f32 v[160:161], v[152:153], v[148:149] op_sel:[0,1] op_sel_hi:[1,0]
	v_pk_mul_f32 v[148:149], v[152:153], v[148:149]
	v_pk_mul_f32 v[162:163], v[154:155], v[150:151] op_sel:[0,1] op_sel_hi:[1,0]
	v_pk_mul_f32 v[150:151], v[154:155], v[150:151]
	s_waitcnt vmcnt(2)
	v_pk_mul_f32 v[164:165], v[156:157], v[130:131] op_sel:[0,1] op_sel_hi:[1,0]
	v_pk_mul_f32 v[130:131], v[156:157], v[130:131]
	v_pk_mul_f32 v[166:167], v[158:159], v[132:133] op_sel:[0,1] op_sel_hi:[1,0]
	v_pk_mul_f32 v[132:133], v[158:159], v[132:133]
	v_sub_f32_e32 v160, v160, v161
	v_add_f32_e32 v148, v149, v148
	v_sub_f32_e32 v149, v162, v163
	v_add_f32_e32 v150, v151, v150
	v_sub_f32_e32 v151, v164, v165
	v_add_f32_e32 v161, v131, v130
	v_sub_f32_e32 v131, v166, v167
	v_lshl_add_u32 v164, v168, 4, 0
	v_add_f32_e32 v132, v133, v132
	v_cvt_pk_f16_f32 v130, v160, v149
	v_cvt_pk_f16_f32 v131, v151, v131
	v_cvt_pk_f16_f32 v148, v148, v150
	v_cvt_pk_f16_f32 v149, v161, v132
	ds_read_b128 v[160:163], v164
	v_mov_b32_e32 v150, v122
	v_mov_b32_e32 v151, v118
	v_mov_b32_e32 v118, v123
	s_waitcnt lgkmcnt(0)
	v_add_f32_e32 v132, v160, v161
	v_add_f32_e32 v132, v162, v132
	v_add_f32_e32 v132, v163, v132
	v_fmamk_f32 v132, v132, 0x3c000000, v147
	v_mul_f32_e32 v133, 0x4b800000, v132
	v_cmp_gt_f32_e32 vcc, s2, v132
	s_nop 1
	v_cndmask_b32_e32 v132, v132, v133, vcc
	v_rsq_f32_e32 v132, v132
	s_nop 0
	v_mul_f32_e32 v133, 0x45800000, v132
	v_cndmask_b32_e32 v132, v132, v133, vcc
	v_pk_mul_f32 v[150:151], v[150:151], v[132:133] op_sel_hi:[1,0]
	s_nop 0
	v_pk_mul_f32 v[150:151], v[128:129], v[150:151]
	s_waitcnt vmcnt(1)
	v_pk_mul_f32 v[160:161], v[138:139], v[150:151] op_sel:[0,1] op_sel_hi:[1,0]
	v_pk_mul_f32 v[150:151], v[138:139], v[150:151]
	v_sub_f32_e32 v133, v160, v161
	v_pk_mul_f32 v[118:119], v[118:119], v[132:133] op_sel_hi:[1,0]
	v_add_f32_e32 v150, v151, v150
	v_pk_mul_f32 v[118:119], v[66:67], v[118:119]
	s_nop 0
	v_pk_mul_f32 v[122:123], v[140:141], v[118:119] op_sel:[0,1] op_sel_hi:[1,0]
	v_pk_mul_f32 v[118:119], v[140:141], v[118:119]
	v_sub_f32_e32 v151, v122, v123
	v_add_f32_e32 v160, v119, v118
	v_mov_b32_e32 v118, v124
	v_mov_b32_e32 v119, v120
	v_pk_mul_f32 v[118:119], v[118:119], v[132:133] op_sel_hi:[1,0]
	v_mov_b32_e32 v120, v125
	v_pk_mul_f32 v[118:119], v[126:127], v[118:119]
	s_waitcnt vmcnt(0)
	v_pk_mul_f32 v[122:123], v[134:135], v[118:119] op_sel:[0,1] op_sel_hi:[1,0]
	v_pk_mul_f32 v[118:119], v[134:135], v[118:119]
	v_sub_f32_e32 v122, v122, v123
	v_add_f32_e32 v123, v119, v118
	v_pk_mul_f32 v[118:119], v[120:121], v[132:133] op_sel_hi:[1,0]
	v_cvt_pk_f16_f32 v132, v133, v151
	s_nop 0
	v_pk_mul_f32 v[118:119], v[68:69], v[118:119]
	v_permlane16_swap_b32_e32 v130, v132
	v_pk_mul_f32 v[120:121], v[136:137], v[118:119] op_sel:[0,1] op_sel_hi:[1,0]
	v_pk_mul_f32 v[118:119], v[136:137], v[118:119]
	v_sub_f32_e32 v120, v120, v121
	v_add_f32_e32 v118, v119, v118
	v_cvt_pk_f16_f32 v133, v122, v120
	v_cvt_pk_f16_f32 v150, v150, v160
	v_cvt_pk_f16_f32 v151, v123, v118
	ds_read_b128 v[118:121], v142 offset:4096
	v_permlane16_swap_b32_e32 v131, v133
	v_permlane16_swap_b32_e32 v148, v150
	s_waitcnt lgkmcnt(0)
	v_add_f32_e32 v118, v118, v119
	v_add_f32_e32 v118, v120, v118
	v_add_f32_e32 v118, v121, v118
	v_fmamk_f32 v118, v118, 0x3c000000, v147
	v_mul_f32_e32 v119, 0x4b800000, v118
	v_cmp_gt_f32_e32 vcc, s2, v118
	v_mov_b32_e32 v120, v114
	v_mov_b32_e32 v121, v110
	v_cndmask_b32_e32 v118, v118, v119, vcc
	v_rsq_f32_e32 v118, v118
	v_mov_b32_e32 v110, v115
	v_permlane16_swap_b32_e32 v149, v151
	v_mul_f32_e32 v119, 0x45800000, v118
	v_cndmask_b32_e32 v118, v118, v119, vcc
	v_pk_mul_f32 v[120:121], v[120:121], v[118:119] op_sel_hi:[1,0]
	global_store_dwordx4 v[0:1], v[130:133], off
	global_store_dwordx4 v[0:1], v[148:151], off offset:128
	v_pk_mul_f32 v[120:121], v[128:129], v[120:121]
	v_or_b32_e32 v130, 32, v146
	v_pk_mul_f32 v[122:123], v[152:153], v[120:121] op_sel:[0,1] op_sel_hi:[1,0]
	v_pk_mul_f32 v[120:121], v[152:153], v[120:121]
	v_sub_f32_e32 v119, v122, v123
	v_pk_mul_f32 v[110:111], v[110:111], v[118:119] op_sel_hi:[1,0]
	v_add_f32_e32 v120, v121, v120
	v_pk_mul_f32 v[110:111], v[66:67], v[110:111]
	s_nop 0
	v_pk_mul_f32 v[114:115], v[154:155], v[110:111] op_sel:[0,1] op_sel_hi:[1,0]
	v_pk_mul_f32 v[110:111], v[154:155], v[110:111]
	v_sub_f32_e32 v121, v114, v115
	v_add_f32_e32 v122, v111, v110
	v_mov_b32_e32 v110, v116
	v_mov_b32_e32 v111, v112
	v_pk_mul_f32 v[110:111], v[110:111], v[118:119] op_sel_hi:[1,0]
	v_mov_b32_e32 v112, v117
	v_pk_mul_f32 v[110:111], v[126:127], v[110:111]
	s_nop 0
	v_pk_mul_f32 v[114:115], v[156:157], v[110:111] op_sel:[0,1] op_sel_hi:[1,0]
	v_pk_mul_f32 v[110:111], v[156:157], v[110:111]
	v_sub_f32_e32 v114, v114, v115
	v_add_f32_e32 v115, v111, v110
	v_pk_mul_f32 v[110:111], v[112:113], v[118:119] op_sel_hi:[1,0]
	s_nop 0
	v_pk_mul_f32 v[110:111], v[68:69], v[110:111]
	s_nop 0
	v_pk_mul_f32 v[112:113], v[158:159], v[110:111] op_sel:[0,1] op_sel_hi:[1,0]
	v_pk_mul_f32 v[110:111], v[158:159], v[110:111]
	v_sub_f32_e32 v112, v112, v113
	v_add_f32_e32 v113, v111, v110
	v_cvt_pk_f16_f32 v110, v119, v121
	v_cvt_pk_f16_f32 v111, v114, v112
	v_cvt_pk_f16_f32 v114, v120, v122
	v_cvt_pk_f16_f32 v115, v115, v113
	ds_read_b128 v[116:119], v164 offset:4096
	s_waitcnt lgkmcnt(0)
	v_add_f32_e32 v112, v116, v117
	v_add_f32_e32 v112, v118, v112
	v_add_f32_e32 v112, v119, v112
	v_fmamk_f32 v112, v112, 0x3c000000, v147
	v_mul_f32_e32 v113, 0x4b800000, v112
	v_cmp_gt_f32_e32 vcc, s2, v112
	v_mov_b32_e32 v116, v106
	v_mov_b32_e32 v117, v102
	v_cndmask_b32_e32 v112, v112, v113, vcc
	v_rsq_f32_e32 v112, v112
	v_mov_b32_e32 v102, v107
	v_mul_f32_e32 v113, 0x45800000, v112
	v_cndmask_b32_e32 v112, v112, v113, vcc
	v_pk_mul_f32 v[116:117], v[116:117], v[112:113] op_sel_hi:[1,0]
	s_nop 0
	v_pk_mul_f32 v[116:117], v[128:129], v[116:117]
	s_nop 0
	v_pk_mul_f32 v[118:119], v[138:139], v[116:117] op_sel:[0,1] op_sel_hi:[1,0]
	v_pk_mul_f32 v[116:117], v[138:139], v[116:117]
	v_sub_f32_e32 v113, v118, v119
	v_pk_mul_f32 v[102:103], v[102:103], v[112:113] op_sel_hi:[1,0]
	v_add_f32_e32 v116, v117, v116
	v_pk_mul_f32 v[102:103], v[66:67], v[102:103]
	s_nop 0
	v_pk_mul_f32 v[106:107], v[140:141], v[102:103] op_sel:[0,1] op_sel_hi:[1,0]
	v_pk_mul_f32 v[102:103], v[140:141], v[102:103]
	v_sub_f32_e32 v117, v106, v107
	v_add_f32_e32 v118, v103, v102
	v_mov_b32_e32 v102, v108
	v_mov_b32_e32 v103, v104
	v_pk_mul_f32 v[102:103], v[102:103], v[112:113] op_sel_hi:[1,0]
	v_mov_b32_e32 v104, v109
	v_pk_mul_f32 v[102:103], v[126:127], v[102:103]
	s_nop 0
	v_pk_mul_f32 v[106:107], v[134:135], v[102:103] op_sel:[0,1] op_sel_hi:[1,0]
	v_pk_mul_f32 v[102:103], v[134:135], v[102:103]
	v_sub_f32_e32 v106, v106, v107
	v_add_f32_e32 v107, v103, v102
	v_pk_mul_f32 v[102:103], v[104:105], v[112:113] op_sel_hi:[1,0]
	v_cvt_pk_f16_f32 v112, v113, v117
	v_or_b32_e32 v134, 48, v146
	v_pk_mul_f32 v[102:103], v[68:69], v[102:103]
	v_lshl_add_u32 v135, v130, 4, 0
	v_pk_mul_f32 v[104:105], v[136:137], v[102:103] op_sel:[0,1] op_sel_hi:[1,0]
	v_pk_mul_f32 v[102:103], v[136:137], v[102:103]
	v_sub_f32_e32 v104, v104, v105
	v_add_f32_e32 v102, v103, v102
	v_cvt_pk_f16_f32 v113, v106, v104
	v_cvt_pk_f16_f32 v116, v116, v118
	v_cvt_pk_f16_f32 v117, v107, v102
	v_or_b32_e32 v102, s3, v130
	v_lshlrev_b32_e32 v102, 9, v102
	v_and_b32_e32 v142, 0xede00, v102
	v_lshl_add_u64 v[102:103], v[144:145], 0, v[142:143]
	global_load_dwordx4 v[106:109], v[102:103], off
	global_load_dwordx4 v[118:121], v[102:103], off offset:16
	v_or_b32_e32 v102, s3, v134
	v_lshlrev_b32_e32 v102, 9, v102
	v_and_b32_e32 v142, 0xefe00, v102
	v_lshl_add_u64 v[122:123], v[144:145], 0, v[142:143]
	global_load_dwordx4 v[102:105], v[122:123], off offset:16
	s_nop 0
	global_load_dwordx4 v[122:125], v[122:123], off
	ds_read_b128 v[130:133], v135
	v_permlane16_swap_b32_e32 v110, v112
	v_permlane16_swap_b32_e32 v111, v113
	s_waitcnt lgkmcnt(0)
	v_add_f32_e32 v130, v130, v131
	v_add_f32_e32 v130, v132, v130
	v_add_f32_e32 v130, v133, v130
	v_fmamk_f32 v130, v130, 0x3c000000, v147
	v_mul_f32_e32 v131, 0x4b800000, v130
	v_cmp_gt_f32_e32 vcc, s2, v130
	v_permlane16_swap_b32_e32 v114, v116
	s_nop 0
	v_cndmask_b32_e32 v130, v130, v131, vcc
	v_rsq_f32_e32 v132, v130
	v_add_co_u32_e64 v130, s[0:1], s0, v0
	v_permlane16_swap_b32_e32 v115, v117
	s_nop 0
	v_addc_co_u32_e64 v131, s[0:1], 0, v1, s[0:1]
	global_store_dwordx4 v[130:131], v[110:113], off
	global_store_dwordx4 v[130:131], v[114:117], off offset:128
	s_movk_i32 s0, 0x2000
	v_mul_f32_e32 v110, 0x45800000, v132
	v_cndmask_b32_e32 v110, v132, v110, vcc
	v_mov_b32_e32 v112, v98
	v_mov_b32_e32 v113, v94
	v_pk_mul_f32 v[112:113], v[112:113], v[110:111] op_sel_hi:[1,0]
	v_mov_b32_e32 v94, v99
	v_pk_mul_f32 v[112:113], v[128:129], v[112:113]
	s_waitcnt vmcnt(5)
	v_pk_mul_f32 v[114:115], v[106:107], v[112:113] op_sel:[0,1] op_sel_hi:[1,0]
	s_nop 0
	v_sub_f32_e32 v111, v114, v115
	v_pk_mul_f32 v[94:95], v[94:95], v[110:111] op_sel_hi:[1,0]
	v_pk_mul_f32 v[112:113], v[106:107], v[112:113]
	v_pk_mul_f32 v[94:95], v[66:67], v[94:95]
	v_add_f32_e32 v112, v113, v112
	v_pk_mul_f32 v[98:99], v[108:109], v[94:95] op_sel:[0,1] op_sel_hi:[1,0]
	v_pk_mul_f32 v[94:95], v[108:109], v[94:95]
	v_sub_f32_e32 v113, v98, v99
	v_add_f32_e32 v114, v95, v94
	v_mov_b32_e32 v94, v100
	v_mov_b32_e32 v95, v96
	v_pk_mul_f32 v[94:95], v[94:95], v[110:111] op_sel_hi:[1,0]
	v_mov_b32_e32 v96, v101
	v_pk_mul_f32 v[94:95], v[126:127], v[94:95]
	v_mov_b32_e32 v100, v90
	s_waitcnt vmcnt(4)
	v_pk_mul_f32 v[98:99], v[118:119], v[94:95] op_sel:[0,1] op_sel_hi:[1,0]
	v_pk_mul_f32 v[94:95], v[118:119], v[94:95]
	v_sub_f32_e32 v98, v98, v99
	v_add_f32_e32 v99, v95, v94
	v_pk_mul_f32 v[94:95], v[96:97], v[110:111] op_sel_hi:[1,0]
	v_mov_b32_e32 v101, v86
	v_pk_mul_f32 v[94:95], v[68:69], v[94:95]
	v_mov_b32_e32 v86, v91
	v_pk_mul_f32 v[96:97], v[120:121], v[94:95] op_sel:[0,1] op_sel_hi:[1,0]
	v_pk_mul_f32 v[94:95], v[120:121], v[94:95]
	v_sub_f32_e32 v96, v96, v97
	v_add_f32_e32 v97, v95, v94
	v_cvt_pk_f16_f32 v94, v111, v113
	v_cvt_pk_f16_f32 v95, v98, v96
	v_cvt_pk_f16_f32 v98, v112, v114
	v_lshl_add_u32 v114, v134, 4, 0
	v_cvt_pk_f16_f32 v99, v99, v97
	ds_read_b128 v[110:113], v114
	s_waitcnt lgkmcnt(0)
	v_add_f32_e32 v96, v110, v111
	v_add_f32_e32 v96, v112, v96
	v_add_f32_e32 v96, v113, v96
	v_fmamk_f32 v96, v96, 0x3c000000, v147
	v_mul_f32_e32 v97, 0x4b800000, v96
	v_cmp_gt_f32_e32 vcc, s2, v96
	s_nop 1
	v_cndmask_b32_e32 v96, v96, v97, vcc
	v_rsq_f32_e32 v96, v96
	s_nop 0
	v_mul_f32_e32 v97, 0x45800000, v96
	v_cndmask_b32_e32 v96, v96, v97, vcc
	v_pk_mul_f32 v[100:101], v[100:101], v[96:97] op_sel_hi:[1,0]
	s_nop 0
	v_pk_mul_f32 v[100:101], v[128:129], v[100:101]
	s_waitcnt vmcnt(2)
	v_pk_mul_f32 v[110:111], v[122:123], v[100:101] op_sel:[0,1] op_sel_hi:[1,0]
	v_pk_mul_f32 v[100:101], v[122:123], v[100:101]
	v_sub_f32_e32 v97, v110, v111
	v_pk_mul_f32 v[86:87], v[86:87], v[96:97] op_sel_hi:[1,0]
	v_add_f32_e32 v100, v101, v100
	v_pk_mul_f32 v[86:87], v[66:67], v[86:87]
	s_nop 0
	v_pk_mul_f32 v[90:91], v[124:125], v[86:87] op_sel:[0,1] op_sel_hi:[1,0]
	v_pk_mul_f32 v[86:87], v[124:125], v[86:87]
	v_sub_f32_e32 v101, v90, v91
	v_add_f32_e32 v110, v87, v86
	v_mov_b32_e32 v86, v92
	v_mov_b32_e32 v87, v88
	v_pk_mul_f32 v[86:87], v[86:87], v[96:97] op_sel_hi:[1,0]
	v_mov_b32_e32 v88, v93
	v_pk_mul_f32 v[86:87], v[126:127], v[86:87]
	s_nop 0
	v_pk_mul_f32 v[90:91], v[102:103], v[86:87] op_sel:[0,1] op_sel_hi:[1,0]
	v_pk_mul_f32 v[86:87], v[102:103], v[86:87]
	v_sub_f32_e32 v90, v90, v91
	v_add_f32_e32 v91, v87, v86
	v_pk_mul_f32 v[86:87], v[88:89], v[96:97] op_sel_hi:[1,0]
	v_cvt_pk_f16_f32 v96, v97, v101
	s_nop 0
	v_pk_mul_f32 v[86:87], v[68:69], v[86:87]
	v_permlane16_swap_b32_e32 v94, v96
	v_pk_mul_f32 v[88:89], v[104:105], v[86:87] op_sel:[0,1] op_sel_hi:[1,0]
	v_pk_mul_f32 v[86:87], v[104:105], v[86:87]
	v_sub_f32_e32 v88, v88, v89
	v_add_f32_e32 v86, v87, v86
	v_cvt_pk_f16_f32 v97, v90, v88
	v_cvt_pk_f16_f32 v100, v100, v110
	v_cvt_pk_f16_f32 v101, v91, v86
	ds_read_b128 v[86:89], v135 offset:4096
	v_permlane16_swap_b32_e32 v95, v97
	v_permlane16_swap_b32_e32 v98, v100
	s_waitcnt lgkmcnt(0)
	v_add_f32_e32 v86, v86, v87
	v_add_f32_e32 v86, v88, v86
	v_add_f32_e32 v86, v89, v86
	v_fmamk_f32 v86, v86, 0x3c000000, v147
	v_mul_f32_e32 v87, 0x4b800000, v86
	v_cmp_gt_f32_e32 vcc, s2, v86
	v_permlane16_swap_b32_e32 v99, v101
	s_nop 0
	v_cndmask_b32_e32 v86, v86, v87, vcc
	v_rsq_f32_e32 v88, v86
	v_add_co_u32_e64 v86, s[0:1], s0, v0
	v_mov_b32_e32 v89, v78
	s_nop 0
	v_addc_co_u32_e64 v87, s[0:1], 0, v1, s[0:1]
	global_store_dwordx4 v[86:87], v[94:97], off
	global_store_dwordx4 v[86:87], v[98:101], off offset:128
	v_mul_f32_e32 v86, 0x45800000, v88
	v_cndmask_b32_e32 v86, v88, v86, vcc
	v_mov_b32_e32 v88, v82
	v_pk_mul_f32 v[88:89], v[88:89], v[86:87] op_sel_hi:[1,0]
	v_mov_b32_e32 v78, v83
	v_pk_mul_f32 v[88:89], v[128:129], v[88:89]
	v_or_b32_e32 v96, 0x80, v146
	v_pk_mul_f32 v[90:91], v[106:107], v[88:89] op_sel:[0,1] op_sel_hi:[1,0]
	v_pk_mul_f32 v[88:89], v[106:107], v[88:89]
	v_sub_f32_e32 v87, v90, v91
	v_pk_mul_f32 v[78:79], v[78:79], v[86:87] op_sel_hi:[1,0]
	v_add_f32_e32 v88, v89, v88
	v_pk_mul_f32 v[78:79], v[66:67], v[78:79]
	v_add_u32_e32 v98, 0x90, v146
	v_pk_mul_f32 v[82:83], v[108:109], v[78:79] op_sel:[0,1] op_sel_hi:[1,0]
	v_pk_mul_f32 v[78:79], v[108:109], v[78:79]
	v_sub_f32_e32 v89, v82, v83
	v_add_f32_e32 v90, v79, v78
	v_mov_b32_e32 v78, v84
	v_mov_b32_e32 v79, v80
	v_pk_mul_f32 v[78:79], v[78:79], v[86:87] op_sel_hi:[1,0]
	v_mov_b32_e32 v80, v85
	v_pk_mul_f32 v[78:79], v[126:127], v[78:79]
	v_lshl_add_u32 v99, v96, 4, 0
	v_pk_mul_f32 v[82:83], v[118:119], v[78:79] op_sel:[0,1] op_sel_hi:[1,0]
	v_pk_mul_f32 v[78:79], v[118:119], v[78:79]
	v_sub_f32_e32 v82, v82, v83
	v_add_f32_e32 v83, v79, v78
	v_pk_mul_f32 v[78:79], v[80:81], v[86:87] op_sel_hi:[1,0]
	s_mov_b32 s0, 0x82000
	v_pk_mul_f32 v[78:79], v[68:69], v[78:79]
	s_nop 0
	v_pk_mul_f32 v[80:81], v[120:121], v[78:79] op_sel:[0,1] op_sel_hi:[1,0]
	v_pk_mul_f32 v[78:79], v[120:121], v[78:79]
	v_sub_f32_e32 v80, v80, v81
	v_add_f32_e32 v81, v79, v78
	v_cvt_pk_f16_f32 v78, v87, v89
	v_cvt_pk_f16_f32 v79, v82, v80
	v_cvt_pk_f16_f32 v82, v88, v90
	v_cvt_pk_f16_f32 v83, v83, v81
	ds_read_b128 v[84:87], v114 offset:4096
	s_waitcnt lgkmcnt(0)
	v_add_f32_e32 v80, v84, v85
	v_add_f32_e32 v80, v86, v80
	v_add_f32_e32 v80, v87, v80
	v_fmamk_f32 v80, v80, 0x3c000000, v147
	v_mul_f32_e32 v81, 0x4b800000, v80
	v_cmp_gt_f32_e32 vcc, s2, v80
	v_mov_b32_e32 v84, v74
	v_mov_b32_e32 v85, v70
	v_cndmask_b32_e32 v80, v80, v81, vcc
	v_rsq_f32_e32 v80, v80
	v_mov_b32_e32 v70, v75
	v_mul_f32_e32 v81, 0x45800000, v80
	v_cndmask_b32_e32 v80, v80, v81, vcc
	v_pk_mul_f32 v[84:85], v[84:85], v[80:81] op_sel_hi:[1,0]
	s_nop 0
	v_pk_mul_f32 v[84:85], v[128:129], v[84:85]
	s_nop 0
	v_pk_mul_f32 v[86:87], v[122:123], v[84:85] op_sel:[0,1] op_sel_hi:[1,0]
	v_pk_mul_f32 v[84:85], v[122:123], v[84:85]
	v_sub_f32_e32 v81, v86, v87
	v_pk_mul_f32 v[70:71], v[70:71], v[80:81] op_sel_hi:[1,0]
	v_add_f32_e32 v84, v85, v84
	v_pk_mul_f32 v[70:71], v[66:67], v[70:71]
	s_nop 0
	v_pk_mul_f32 v[74:75], v[124:125], v[70:71] op_sel:[0,1] op_sel_hi:[1,0]
	v_pk_mul_f32 v[70:71], v[124:125], v[70:71]
	v_sub_f32_e32 v85, v74, v75
	v_add_f32_e32 v86, v71, v70
	v_mov_b32_e32 v70, v76
	v_mov_b32_e32 v71, v72
	v_pk_mul_f32 v[70:71], v[70:71], v[80:81] op_sel_hi:[1,0]
	v_mov_b32_e32 v72, v77
	v_pk_mul_f32 v[70:71], v[126:127], v[70:71]
	s_nop 0
	v_pk_mul_f32 v[74:75], v[102:103], v[70:71] op_sel:[0,1] op_sel_hi:[1,0]
	v_pk_mul_f32 v[70:71], v[102:103], v[70:71]
	v_sub_f32_e32 v74, v74, v75
	v_add_f32_e32 v75, v71, v70
	v_pk_mul_f32 v[70:71], v[72:73], v[80:81] op_sel_hi:[1,0]
	v_cvt_pk_f16_f32 v80, v81, v85
	s_nop 0
	v_pk_mul_f32 v[70:71], v[68:69], v[70:71]
	v_permlane16_swap_b32_e32 v78, v80
	v_pk_mul_f32 v[72:73], v[104:105], v[70:71] op_sel:[0,1] op_sel_hi:[1,0]
	v_pk_mul_f32 v[70:71], v[104:105], v[70:71]
	v_sub_f32_e32 v72, v72, v73
	v_add_f32_e32 v70, v71, v70
	v_cvt_pk_f16_f32 v81, v74, v72
	v_cvt_pk_f16_f32 v84, v84, v86
	v_cvt_pk_f16_f32 v85, v75, v70
	v_or_b32_e32 v70, s3, v96
	v_lshlrev_b32_e32 v70, 9, v70
	v_and_b32_e32 v142, 0xf9e00, v70
	v_lshl_add_u64 v[70:71], v[144:145], 0, v[142:143]
	global_load_dwordx4 v[74:77], v[70:71], off
	global_load_dwordx4 v[86:89], v[70:71], off offset:16
	v_add_lshl_u32 v70, s3, v98, 9
	v_and_b32_e32 v142, 0xfbe00, v70
	v_lshl_add_u64 v[94:95], v[144:145], 0, v[142:143]
	global_load_dwordx4 v[70:73], v[94:95], off offset:16
	global_load_dwordx4 v[90:93], v[94:95], off
	ds_read_b128 v[94:97], v99
	v_permlane16_swap_b32_e32 v79, v81
	v_permlane16_swap_b32_e32 v82, v84
	s_waitcnt lgkmcnt(0)
	v_add_f32_e32 v94, v94, v95
	v_add_f32_e32 v94, v96, v94
	v_add_f32_e32 v94, v97, v94
	v_fmamk_f32 v94, v94, 0x3c000000, v147
	v_mul_f32_e32 v95, 0x4b800000, v94
	v_cmp_gt_f32_e32 vcc, s2, v94
	v_permlane16_swap_b32_e32 v83, v85
	s_nop 0
	v_cndmask_b32_e32 v94, v94, v95, vcc
	v_rsq_f32_e32 v96, v94
	v_add_co_u32_e64 v94, s[0:1], s0, v0
	s_nop 1
	v_addc_co_u32_e64 v95, s[0:1], 0, v1, s[0:1]
	global_store_dwordx4 v[94:95], v[78:81], off
	global_store_dwordx4 v[94:95], v[82:85], off offset:128
	s_mov_b32 s0, 0x8000
	v_mul_f32_e32 v78, 0x45800000, v96
	v_cndmask_b32_e32 v78, v96, v78, vcc
	v_mov_b32_e32 v80, v62
	v_mov_b32_e32 v81, v58
	v_pk_mul_f32 v[80:81], v[80:81], v[78:79] op_sel_hi:[1,0]
	v_mov_b32_e32 v58, v63
	v_pk_mul_f32 v[80:81], v[128:129], v[80:81]
	s_waitcnt vmcnt(5)
	v_pk_mul_f32 v[82:83], v[74:75], v[80:81] op_sel:[0,1] op_sel_hi:[1,0]
	s_nop 0
	v_sub_f32_e32 v79, v82, v83
	v_pk_mul_f32 v[58:59], v[58:59], v[78:79] op_sel_hi:[1,0]
	v_pk_mul_f32 v[80:81], v[74:75], v[80:81]
	v_pk_mul_f32 v[58:59], v[66:67], v[58:59]
	v_add_f32_e32 v80, v81, v80
	v_pk_mul_f32 v[62:63], v[76:77], v[58:59] op_sel:[0,1] op_sel_hi:[1,0]
	v_pk_mul_f32 v[58:59], v[76:77], v[58:59]
	v_sub_f32_e32 v81, v62, v63
	v_add_f32_e32 v82, v59, v58
	v_mov_b32_e32 v58, v64
	v_mov_b32_e32 v59, v60
	v_pk_mul_f32 v[58:59], v[58:59], v[78:79] op_sel_hi:[1,0]
	v_mov_b32_e32 v60, v65
	v_pk_mul_f32 v[58:59], v[126:127], v[58:59]
	v_mov_b32_e32 v64, v54
	s_waitcnt vmcnt(4)
	v_pk_mul_f32 v[62:63], v[86:87], v[58:59] op_sel:[0,1] op_sel_hi:[1,0]
	v_pk_mul_f32 v[58:59], v[86:87], v[58:59]
	v_sub_f32_e32 v62, v62, v63
	v_add_f32_e32 v63, v59, v58
	v_pk_mul_f32 v[58:59], v[60:61], v[78:79] op_sel_hi:[1,0]
	v_mov_b32_e32 v65, v50
	v_pk_mul_f32 v[58:59], v[68:69], v[58:59]
	v_mov_b32_e32 v50, v55
	v_pk_mul_f32 v[60:61], v[88:89], v[58:59] op_sel:[0,1] op_sel_hi:[1,0]
	v_pk_mul_f32 v[58:59], v[88:89], v[58:59]
	v_sub_f32_e32 v60, v60, v61
	v_add_f32_e32 v61, v59, v58
	v_cvt_pk_f16_f32 v58, v79, v81
	v_cvt_pk_f16_f32 v59, v62, v60
	v_cvt_pk_f16_f32 v62, v80, v82
	v_lshl_add_u32 v82, v98, 4, 0
	v_cvt_pk_f16_f32 v63, v63, v61
	ds_read_b128 v[78:81], v82
	s_waitcnt lgkmcnt(0)
	v_add_f32_e32 v60, v78, v79
	v_add_f32_e32 v60, v80, v60
	v_add_f32_e32 v60, v81, v60
	v_fmamk_f32 v60, v60, 0x3c000000, v147
	v_mul_f32_e32 v61, 0x4b800000, v60
	v_cmp_gt_f32_e32 vcc, s2, v60
	s_nop 1
	v_cndmask_b32_e32 v60, v60, v61, vcc
	v_rsq_f32_e32 v60, v60
	s_nop 0
	v_mul_f32_e32 v61, 0x45800000, v60
	v_cndmask_b32_e32 v60, v60, v61, vcc
	v_pk_mul_f32 v[64:65], v[64:65], v[60:61] op_sel_hi:[1,0]
	s_nop 0
	v_pk_mul_f32 v[64:65], v[128:129], v[64:65]
	s_waitcnt vmcnt(2)
	v_pk_mul_f32 v[78:79], v[90:91], v[64:65] op_sel:[0,1] op_sel_hi:[1,0]
	v_pk_mul_f32 v[64:65], v[90:91], v[64:65]
	v_sub_f32_e32 v61, v78, v79
	v_pk_mul_f32 v[50:51], v[50:51], v[60:61] op_sel_hi:[1,0]
	v_add_f32_e32 v64, v65, v64
	v_pk_mul_f32 v[50:51], v[66:67], v[50:51]
	s_nop 0
	v_pk_mul_f32 v[54:55], v[92:93], v[50:51] op_sel:[0,1] op_sel_hi:[1,0]
	v_pk_mul_f32 v[50:51], v[92:93], v[50:51]
	v_sub_f32_e32 v65, v54, v55
	v_add_f32_e32 v78, v51, v50
	v_mov_b32_e32 v50, v56
	v_mov_b32_e32 v51, v52
	v_pk_mul_f32 v[50:51], v[50:51], v[60:61] op_sel_hi:[1,0]
	v_mov_b32_e32 v52, v57
	v_pk_mul_f32 v[50:51], v[126:127], v[50:51]
	s_nop 0
	v_pk_mul_f32 v[54:55], v[70:71], v[50:51] op_sel:[0,1] op_sel_hi:[1,0]
	v_pk_mul_f32 v[50:51], v[70:71], v[50:51]
	v_sub_f32_e32 v54, v54, v55
	v_add_f32_e32 v55, v51, v50
	v_pk_mul_f32 v[50:51], v[52:53], v[60:61] op_sel_hi:[1,0]
	v_cvt_pk_f16_f32 v60, v61, v65
	s_nop 0
	v_pk_mul_f32 v[50:51], v[68:69], v[50:51]
	v_permlane16_swap_b32_e32 v58, v60
	v_pk_mul_f32 v[52:53], v[72:73], v[50:51] op_sel:[0,1] op_sel_hi:[1,0]
	v_pk_mul_f32 v[50:51], v[72:73], v[50:51]
	v_sub_f32_e32 v52, v52, v53
	v_add_f32_e32 v50, v51, v50
	v_cvt_pk_f16_f32 v61, v54, v52
	v_cvt_pk_f16_f32 v64, v64, v78
	v_cvt_pk_f16_f32 v65, v55, v50
	ds_read_b128 v[50:53], v99 offset:4096
	v_permlane16_swap_b32_e32 v59, v61
	v_permlane16_swap_b32_e32 v62, v64
	s_waitcnt lgkmcnt(0)
	v_add_f32_e32 v50, v50, v51
	v_add_f32_e32 v50, v52, v50
	v_add_f32_e32 v50, v53, v50
	v_fmamk_f32 v50, v50, 0x3c000000, v147
	v_mul_f32_e32 v51, 0x4b800000, v50
	v_cmp_gt_f32_e32 vcc, s2, v50
	v_permlane16_swap_b32_e32 v63, v65
	s_nop 0
	v_cndmask_b32_e32 v50, v50, v51, vcc
	v_rsq_f32_e32 v52, v50
	v_add_co_u32_e64 v50, s[0:1], s0, v0
	v_mov_b32_e32 v53, v42
	s_nop 0
	v_addc_co_u32_e64 v51, s[0:1], 0, v1, s[0:1]
	global_store_dwordx4 v[50:51], v[58:61], off
	global_store_dwordx4 v[50:51], v[62:65], off offset:128
	v_mul_f32_e32 v50, 0x45800000, v52
	v_cndmask_b32_e32 v50, v52, v50, vcc
	v_mov_b32_e32 v52, v46
	v_pk_mul_f32 v[52:53], v[52:53], v[50:51] op_sel_hi:[1,0]
	v_mov_b32_e32 v42, v47
	v_pk_mul_f32 v[52:53], v[128:129], v[52:53]
	v_add_u32_e32 v60, 0xa0, v146
	v_pk_mul_f32 v[54:55], v[74:75], v[52:53] op_sel:[0,1] op_sel_hi:[1,0]
	v_pk_mul_f32 v[52:53], v[74:75], v[52:53]
	v_sub_f32_e32 v51, v54, v55
	v_pk_mul_f32 v[42:43], v[42:43], v[50:51] op_sel_hi:[1,0]
	v_add_f32_e32 v52, v53, v52
	v_pk_mul_f32 v[42:43], v[66:67], v[42:43]
	v_add_u32_e32 v62, 0xb0, v146
	v_pk_mul_f32 v[46:47], v[76:77], v[42:43] op_sel:[0,1] op_sel_hi:[1,0]
	v_pk_mul_f32 v[42:43], v[76:77], v[42:43]
	v_sub_f32_e32 v53, v46, v47
	v_add_f32_e32 v54, v43, v42
	v_mov_b32_e32 v42, v48
	v_mov_b32_e32 v43, v44
	v_pk_mul_f32 v[42:43], v[42:43], v[50:51] op_sel_hi:[1,0]
	v_mov_b32_e32 v44, v49
	v_pk_mul_f32 v[42:43], v[126:127], v[42:43]
	v_lshl_add_u32 v63, v60, 4, 0
	v_pk_mul_f32 v[46:47], v[86:87], v[42:43] op_sel:[0,1] op_sel_hi:[1,0]
	v_pk_mul_f32 v[42:43], v[86:87], v[42:43]
	v_sub_f32_e32 v46, v46, v47
	v_add_f32_e32 v47, v43, v42
	v_pk_mul_f32 v[42:43], v[44:45], v[50:51] op_sel_hi:[1,0]
	s_mov_b32 s0, 0x88000
	v_pk_mul_f32 v[42:43], v[68:69], v[42:43]
	s_nop 0
	v_pk_mul_f32 v[44:45], v[88:89], v[42:43] op_sel:[0,1] op_sel_hi:[1,0]
	v_pk_mul_f32 v[42:43], v[88:89], v[42:43]
	v_sub_f32_e32 v44, v44, v45
	v_add_f32_e32 v45, v43, v42
	v_cvt_pk_f16_f32 v42, v51, v53
	v_cvt_pk_f16_f32 v43, v46, v44
	v_cvt_pk_f16_f32 v46, v52, v54
	v_cvt_pk_f16_f32 v47, v47, v45
	ds_read_b128 v[48:51], v82 offset:4096
	s_waitcnt lgkmcnt(0)
	v_add_f32_e32 v44, v48, v49
	v_add_f32_e32 v44, v50, v44
	v_add_f32_e32 v44, v51, v44
	v_fmamk_f32 v44, v44, 0x3c000000, v147
	v_mul_f32_e32 v45, 0x4b800000, v44
	v_cmp_gt_f32_e32 vcc, s2, v44
	v_mov_b32_e32 v48, v38
	v_mov_b32_e32 v49, v34
	v_cndmask_b32_e32 v44, v44, v45, vcc
	v_rsq_f32_e32 v44, v44
	v_mov_b32_e32 v34, v39
	v_mul_f32_e32 v45, 0x45800000, v44
	v_cndmask_b32_e32 v44, v44, v45, vcc
	v_pk_mul_f32 v[48:49], v[48:49], v[44:45] op_sel_hi:[1,0]
	s_nop 0
	v_pk_mul_f32 v[48:49], v[128:129], v[48:49]
	s_nop 0
	v_pk_mul_f32 v[50:51], v[90:91], v[48:49] op_sel:[0,1] op_sel_hi:[1,0]
	v_pk_mul_f32 v[48:49], v[90:91], v[48:49]
	v_sub_f32_e32 v45, v50, v51
	v_pk_mul_f32 v[34:35], v[34:35], v[44:45] op_sel_hi:[1,0]
	v_add_f32_e32 v48, v49, v48
	v_pk_mul_f32 v[34:35], v[66:67], v[34:35]
	s_nop 0
	v_pk_mul_f32 v[38:39], v[92:93], v[34:35] op_sel:[0,1] op_sel_hi:[1,0]
	v_pk_mul_f32 v[34:35], v[92:93], v[34:35]
	v_sub_f32_e32 v49, v38, v39
	v_add_f32_e32 v50, v35, v34
	v_mov_b32_e32 v34, v40
	v_mov_b32_e32 v35, v36
	v_pk_mul_f32 v[34:35], v[34:35], v[44:45] op_sel_hi:[1,0]
	v_mov_b32_e32 v36, v41
	v_pk_mul_f32 v[34:35], v[126:127], v[34:35]
	s_nop 0
	v_pk_mul_f32 v[38:39], v[70:71], v[34:35] op_sel:[0,1] op_sel_hi:[1,0]
	v_pk_mul_f32 v[34:35], v[70:71], v[34:35]
	v_sub_f32_e32 v38, v38, v39
	v_add_f32_e32 v39, v35, v34
	v_pk_mul_f32 v[34:35], v[36:37], v[44:45] op_sel_hi:[1,0]
	v_cvt_pk_f16_f32 v44, v45, v49
	s_nop 0
	v_pk_mul_f32 v[34:35], v[68:69], v[34:35]
	v_permlane16_swap_b32_e32 v42, v44
	v_pk_mul_f32 v[36:37], v[72:73], v[34:35] op_sel:[0,1] op_sel_hi:[1,0]
	v_pk_mul_f32 v[34:35], v[72:73], v[34:35]
	v_sub_f32_e32 v36, v36, v37
	v_add_f32_e32 v34, v35, v34
	v_cvt_pk_f16_f32 v45, v38, v36
	v_cvt_pk_f16_f32 v48, v48, v50
	v_cvt_pk_f16_f32 v49, v39, v34
	v_add_lshl_u32 v34, s3, v60, 9
	v_and_b32_e32 v142, 0xfde00, v34
	v_lshl_add_u64 v[34:35], v[144:145], 0, v[142:143]
	global_load_dwordx4 v[38:41], v[34:35], off
	global_load_dwordx4 v[50:53], v[34:35], off offset:16
	v_add_lshl_u32 v34, s3, v62, 9
	v_and_b32_e32 v142, 0xffe00, v34
	v_lshl_add_u64 v[58:59], v[144:145], 0, v[142:143]
	global_load_dwordx4 v[34:37], v[58:59], off offset:16
	global_load_dwordx4 v[54:57], v[58:59], off
	ds_read_b128 v[58:61], v63
	v_permlane16_swap_b32_e32 v43, v45
	v_permlane16_swap_b32_e32 v46, v48
	s_waitcnt lgkmcnt(0)
	v_add_f32_e32 v58, v58, v59
	v_add_f32_e32 v58, v60, v58
	v_add_f32_e32 v58, v61, v58
	v_fmamk_f32 v58, v58, 0x3c000000, v147
	v_mul_f32_e32 v59, 0x4b800000, v58
	v_cmp_gt_f32_e32 vcc, s2, v58
	v_permlane16_swap_b32_e32 v47, v49
	s_nop 0
	v_cndmask_b32_e32 v58, v58, v59, vcc
	v_rsq_f32_e32 v60, v58
	v_add_co_u32_e64 v58, s[0:1], s0, v0
	s_nop 1
	v_addc_co_u32_e64 v59, s[0:1], 0, v1, s[0:1]
	global_store_dwordx4 v[58:59], v[42:45], off
	global_store_dwordx4 v[58:59], v[46:49], off offset:128
	s_mov_b32 s0, 0xa000
	v_mul_f32_e32 v42, 0x45800000, v60
	v_cndmask_b32_e32 v42, v60, v42, vcc
	v_mov_b32_e32 v44, v30
	v_mov_b32_e32 v45, v26
	v_pk_mul_f32 v[44:45], v[44:45], v[42:43] op_sel_hi:[1,0]
	v_mov_b32_e32 v26, v31
	v_pk_mul_f32 v[44:45], v[128:129], v[44:45]
	s_waitcnt vmcnt(5)
	v_pk_mul_f32 v[46:47], v[38:39], v[44:45] op_sel:[0,1] op_sel_hi:[1,0]
	s_nop 0
	v_sub_f32_e32 v43, v46, v47
	v_pk_mul_f32 v[26:27], v[26:27], v[42:43] op_sel_hi:[1,0]
	v_pk_mul_f32 v[44:45], v[38:39], v[44:45]
	v_pk_mul_f32 v[26:27], v[66:67], v[26:27]
	v_add_f32_e32 v44, v45, v44
	v_pk_mul_f32 v[30:31], v[40:41], v[26:27] op_sel:[0,1] op_sel_hi:[1,0]
	v_pk_mul_f32 v[26:27], v[40:41], v[26:27]
	v_sub_f32_e32 v45, v30, v31
	v_add_f32_e32 v46, v27, v26
	v_mov_b32_e32 v26, v32
	v_mov_b32_e32 v27, v28
	v_pk_mul_f32 v[26:27], v[26:27], v[42:43] op_sel_hi:[1,0]
	v_mov_b32_e32 v28, v33
	v_pk_mul_f32 v[26:27], v[126:127], v[26:27]
	v_mov_b32_e32 v32, v22
	s_waitcnt vmcnt(4)
	v_pk_mul_f32 v[30:31], v[50:51], v[26:27] op_sel:[0,1] op_sel_hi:[1,0]
	v_pk_mul_f32 v[26:27], v[50:51], v[26:27]
	v_sub_f32_e32 v30, v30, v31
	v_add_f32_e32 v31, v27, v26
	v_pk_mul_f32 v[26:27], v[28:29], v[42:43] op_sel_hi:[1,0]
	v_mov_b32_e32 v33, v18
	v_pk_mul_f32 v[26:27], v[68:69], v[26:27]
	v_mov_b32_e32 v18, v23
	v_pk_mul_f32 v[28:29], v[52:53], v[26:27] op_sel:[0,1] op_sel_hi:[1,0]
	v_pk_mul_f32 v[26:27], v[52:53], v[26:27]
	v_sub_f32_e32 v28, v28, v29
	v_add_f32_e32 v29, v27, v26
	v_cvt_pk_f16_f32 v26, v43, v45
	v_cvt_pk_f16_f32 v27, v30, v28
	v_cvt_pk_f16_f32 v30, v44, v46
	v_lshl_add_u32 v46, v62, 4, 0
	v_cvt_pk_f16_f32 v31, v31, v29
	ds_read_b128 v[42:45], v46
	s_waitcnt lgkmcnt(0)
	v_add_f32_e32 v28, v42, v43
	v_add_f32_e32 v28, v44, v28
	v_add_f32_e32 v28, v45, v28
	v_fmamk_f32 v28, v28, 0x3c000000, v147
	v_mul_f32_e32 v29, 0x4b800000, v28
	v_cmp_gt_f32_e32 vcc, s2, v28
	s_nop 1
	v_cndmask_b32_e32 v28, v28, v29, vcc
	v_rsq_f32_e32 v28, v28
	s_nop 0
	v_mul_f32_e32 v29, 0x45800000, v28
	v_cndmask_b32_e32 v28, v28, v29, vcc
	v_pk_mul_f32 v[32:33], v[32:33], v[28:29] op_sel_hi:[1,0]
	s_nop 0
	v_pk_mul_f32 v[32:33], v[128:129], v[32:33]
	s_waitcnt vmcnt(2)
	v_pk_mul_f32 v[42:43], v[54:55], v[32:33] op_sel:[0,1] op_sel_hi:[1,0]
	v_pk_mul_f32 v[32:33], v[54:55], v[32:33]
	v_sub_f32_e32 v29, v42, v43
	v_pk_mul_f32 v[18:19], v[18:19], v[28:29] op_sel_hi:[1,0]
	v_add_f32_e32 v32, v33, v32
	v_pk_mul_f32 v[18:19], v[66:67], v[18:19]
	s_nop 0
	v_pk_mul_f32 v[22:23], v[56:57], v[18:19] op_sel:[0,1] op_sel_hi:[1,0]
	v_pk_mul_f32 v[18:19], v[56:57], v[18:19]
	v_sub_f32_e32 v33, v22, v23
	v_add_f32_e32 v42, v19, v18
	v_mov_b32_e32 v18, v24
	v_mov_b32_e32 v19, v20
	v_pk_mul_f32 v[18:19], v[18:19], v[28:29] op_sel_hi:[1,0]
	v_mov_b32_e32 v20, v25
	v_pk_mul_f32 v[18:19], v[126:127], v[18:19]
	s_nop 0
	v_pk_mul_f32 v[22:23], v[34:35], v[18:19] op_sel:[0,1] op_sel_hi:[1,0]
	v_pk_mul_f32 v[18:19], v[34:35], v[18:19]
	v_sub_f32_e32 v22, v22, v23
	v_add_f32_e32 v23, v19, v18
	v_pk_mul_f32 v[18:19], v[20:21], v[28:29] op_sel_hi:[1,0]
	v_cvt_pk_f16_f32 v28, v29, v33
	s_nop 0
	v_pk_mul_f32 v[18:19], v[68:69], v[18:19]
	v_permlane16_swap_b32_e32 v26, v28
	v_pk_mul_f32 v[20:21], v[36:37], v[18:19] op_sel:[0,1] op_sel_hi:[1,0]
	v_pk_mul_f32 v[18:19], v[36:37], v[18:19]
	v_sub_f32_e32 v20, v20, v21
	v_add_f32_e32 v18, v19, v18
	v_cvt_pk_f16_f32 v29, v22, v20
	v_cvt_pk_f16_f32 v32, v32, v42
	v_cvt_pk_f16_f32 v33, v23, v18
	ds_read_b128 v[18:21], v63 offset:4096
	v_permlane16_swap_b32_e32 v27, v29
	v_permlane16_swap_b32_e32 v30, v32
	s_waitcnt lgkmcnt(0)
	v_add_f32_e32 v18, v18, v19
	v_add_f32_e32 v18, v20, v18
	v_add_f32_e32 v18, v21, v18
	v_fmamk_f32 v18, v18, 0x3c000000, v147
	v_mul_f32_e32 v19, 0x4b800000, v18
	v_cmp_gt_f32_e32 vcc, s2, v18
	v_permlane16_swap_b32_e32 v31, v33
	s_nop 0
	v_cndmask_b32_e32 v18, v18, v19, vcc
	v_rsq_f32_e32 v20, v18
	v_add_co_u32_e64 v18, s[0:1], s0, v0
	v_mov_b32_e32 v21, v10
	s_nop 0
	v_addc_co_u32_e64 v19, s[0:1], 0, v1, s[0:1]
	global_store_dwordx4 v[18:19], v[26:29], off
	global_store_dwordx4 v[18:19], v[30:33], off offset:128
	v_mul_f32_e32 v18, 0x45800000, v20
	v_cndmask_b32_e32 v18, v20, v18, vcc
	v_mov_b32_e32 v20, v14
	v_pk_mul_f32 v[20:21], v[20:21], v[18:19] op_sel_hi:[1,0]
	v_mov_b32_e32 v10, v15
	v_pk_mul_f32 v[20:21], v[128:129], v[20:21]
	s_nop 0
	v_pk_mul_f32 v[22:23], v[38:39], v[20:21] op_sel:[0,1] op_sel_hi:[1,0]
	v_pk_mul_f32 v[20:21], v[38:39], v[20:21]
	v_sub_f32_e32 v19, v22, v23
	v_pk_mul_f32 v[10:11], v[10:11], v[18:19] op_sel_hi:[1,0]
	v_add_f32_e32 v20, v21, v20
	v_pk_mul_f32 v[10:11], v[66:67], v[10:11]
	s_nop 0
	v_pk_mul_f32 v[14:15], v[40:41], v[10:11] op_sel:[0,1] op_sel_hi:[1,0]
	v_pk_mul_f32 v[10:11], v[40:41], v[10:11]
	v_sub_f32_e32 v21, v14, v15
	v_add_f32_e32 v22, v11, v10
	v_mov_b32_e32 v10, v16
	v_mov_b32_e32 v11, v12
	v_pk_mul_f32 v[10:11], v[10:11], v[18:19] op_sel_hi:[1,0]
	v_mov_b32_e32 v12, v17
	v_pk_mul_f32 v[10:11], v[126:127], v[10:11]
	s_nop 0
	v_pk_mul_f32 v[14:15], v[50:51], v[10:11] op_sel:[0,1] op_sel_hi:[1,0]
	v_pk_mul_f32 v[10:11], v[50:51], v[10:11]
	v_sub_f32_e32 v14, v14, v15
	v_add_f32_e32 v15, v11, v10
	v_pk_mul_f32 v[10:11], v[12:13], v[18:19] op_sel_hi:[1,0]
	s_nop 0
	v_pk_mul_f32 v[10:11], v[68:69], v[10:11]
	s_nop 0
	v_pk_mul_f32 v[12:13], v[52:53], v[10:11] op_sel:[0,1] op_sel_hi:[1,0]
	v_pk_mul_f32 v[10:11], v[52:53], v[10:11]
	v_sub_f32_e32 v12, v12, v13
	v_add_f32_e32 v13, v11, v10
	v_cvt_pk_f16_f32 v10, v19, v21
	v_cvt_pk_f16_f32 v11, v14, v12
	v_cvt_pk_f16_f32 v14, v20, v22
	v_cvt_pk_f16_f32 v15, v15, v13
	ds_read_b128 v[16:19], v46 offset:4096
	s_waitcnt lgkmcnt(0)
	v_add_f32_e32 v12, v16, v17
	v_add_f32_e32 v12, v18, v12
	v_add_f32_e32 v12, v19, v12
	v_fmac_f32_e32 v147, 0x3c000000, v12
	v_mul_f32_e32 v12, 0x4b800000, v147
	v_cmp_gt_f32_e32 vcc, s2, v147
	v_mov_b32_e32 v16, v6
	v_mov_b32_e32 v17, v2
	v_cndmask_b32_e32 v12, v147, v12, vcc
	v_rsq_f32_e32 v12, v12
	v_mov_b32_e32 v2, v7
	v_mul_f32_e32 v13, 0x45800000, v12
	v_cndmask_b32_e32 v12, v12, v13, vcc
	v_pk_mul_f32 v[16:17], v[16:17], v[12:13] op_sel_hi:[1,0]
	v_add_co_u32_e32 v0, vcc, 0x8a000, v0
	v_pk_mul_f32 v[16:17], v[128:129], v[16:17]
	s_nop 0
	v_addc_co_u32_e32 v1, vcc, 0, v1, vcc
	v_pk_mul_f32 v[18:19], v[54:55], v[16:17] op_sel:[0,1] op_sel_hi:[1,0]
	v_pk_mul_f32 v[16:17], v[54:55], v[16:17]
	v_sub_f32_e32 v13, v18, v19
	v_pk_mul_f32 v[2:3], v[2:3], v[12:13] op_sel_hi:[1,0]
	v_add_f32_e32 v16, v17, v16
	v_pk_mul_f32 v[2:3], v[66:67], v[2:3]
	s_nop 0
	v_pk_mul_f32 v[6:7], v[56:57], v[2:3] op_sel:[0,1] op_sel_hi:[1,0]
	v_pk_mul_f32 v[2:3], v[56:57], v[2:3]
	v_sub_f32_e32 v17, v6, v7
	v_add_f32_e32 v18, v3, v2
	v_mov_b32_e32 v2, v8
	v_mov_b32_e32 v3, v4
	v_pk_mul_f32 v[2:3], v[2:3], v[12:13] op_sel_hi:[1,0]
	v_mov_b32_e32 v4, v9
	v_pk_mul_f32 v[2:3], v[126:127], v[2:3]
	s_nop 0
	v_pk_mul_f32 v[6:7], v[34:35], v[2:3] op_sel:[0,1] op_sel_hi:[1,0]
	v_pk_mul_f32 v[2:3], v[34:35], v[2:3]
	v_sub_f32_e32 v6, v6, v7
	v_add_f32_e32 v7, v3, v2
	v_pk_mul_f32 v[2:3], v[4:5], v[12:13] op_sel_hi:[1,0]
	v_cvt_pk_f16_f32 v12, v13, v17
	s_nop 0
	v_pk_mul_f32 v[2:3], v[68:69], v[2:3]
	v_permlane16_swap_b32_e32 v10, v12
	v_pk_mul_f32 v[4:5], v[36:37], v[2:3] op_sel:[0,1] op_sel_hi:[1,0]
	v_pk_mul_f32 v[2:3], v[36:37], v[2:3]
	v_sub_f32_e32 v4, v4, v5
	v_cvt_pk_f16_f32 v13, v6, v4
	v_add_f32_e32 v2, v3, v2
	v_cvt_pk_f16_f32 v16, v16, v18
	v_cvt_pk_f16_f32 v17, v7, v2
	v_permlane16_swap_b32_e32 v11, v13
	v_permlane16_swap_b32_e32 v14, v16
	v_permlane16_swap_b32_e32 v15, v17
	global_store_dwordx4 v[0:1], v[10:13], off
	global_store_dwordx4 v[0:1], v[14:17], off offset:128
	s_mov_b64 exec, s[56:57]
	s_cbranch_execz .Lkv_noarrive
	v_mov_b32_e32 v228, 0
	v_mov_b32_e32 v229, 1
	global_atomic_add v228, v229, s[54:55] sc1

	.amdhsa_kernel _Z15gemm_qkv_kernelPKDF16_S0_PDF16_PKfS3_PK15HIP_vector_typeIfLj2EE
		.amdhsa_group_segment_fixed_size 0
		.amdhsa_private_segment_fixed_size 0
		.amdhsa_kernarg_size 48
		.amdhsa_user_sgpr_count 2
		.amdhsa_user_sgpr_dispatch_ptr 0
		.amdhsa_user_sgpr_queue_ptr 0
		.amdhsa_user_sgpr_kernarg_segment_ptr 1
		.amdhsa_user_sgpr_dispatch_id 0
		.amdhsa_user_sgpr_kernarg_preload_length 0
		.amdhsa_user_sgpr_kernarg_preload_offset 0
		.amdhsa_user_sgpr_private_segment_size 0
		.amdhsa_uses_dynamic_stack 0
		.amdhsa_enable_private_segment 0
		.amdhsa_system_sgpr_workgroup_id_x 1
		.amdhsa_system_sgpr_workgroup_id_y 0
		.amdhsa_system_sgpr_workgroup_id_z 0
		.amdhsa_system_sgpr_workgroup_info 0
		.amdhsa_system_vgpr_workitem_id 0
		.amdhsa_next_free_vgpr 236
		.amdhsa_next_free_sgpr 58
		.amdhsa_accum_offset 236
		.amdhsa_reserve_vcc 1
		.amdhsa_float_round_mode_32 0
		.amdhsa_float_round_mode_16_64 0
		.amdhsa_float_denorm_mode_32 3
		.amdhsa_float_denorm_mode_16_64 3
		.amdhsa_dx10_clamp 1
		.amdhsa_ieee_mode 1
		.amdhsa_fp16_overflow 0
		.amdhsa_tg_split 0
		.amdhsa_exception_fp_ieee_invalid_op 0
		.amdhsa_exception_fp_denorm_src 0
		.amdhsa_exception_fp_ieee_div_zero 0
		.amdhsa_exception_fp_ieee_overflow 0
		.amdhsa_exception_fp_ieee_underflow 0
		.amdhsa_exception_fp_ieee_inexact 0
		.amdhsa_exception_int_div_zero 0
	.end_amdhsa_kernel

.LBB3_14:
	s_nop 8
	v_max_f32_e32 v2, v21, v21
	v_max_f32_e32 v36, v20, v20
	v_max_f32_e32 v2, v36, v2
	v_max3_f32 v2, v2, v22, v23
	v_max3_f32 v2, v2, v24, v25
	v_max3_f32 v2, v2, v26, v27
	v_max3_f32 v2, v2, v28, v29
	v_max3_f32 v2, v2, v30, v31
	v_max3_f32 v2, v2, v32, v33
	v_max3_f32 v2, v2, v34, v35
	v_max3_f32 v2, v2, v4, v5
	v_max3_f32 v2, v2, v6, v7
	v_max3_f32 v2, v2, v8, v9
	v_max3_f32 v2, v2, v10, v11
	v_max3_f32 v2, v2, v12, v13
	v_max3_f32 v2, v2, v14, v15
	v_max3_f32 v2, v2, v16, v17
	v_max3_f32 v2, v2, v18, v19
	v_mov_b32_e32 v36, v2
	s_nop 1
	v_permlane32_swap_b32_e32 v2, v36
	v_max_f32_e32 v36, v36, v36
	v_max_f32_e32 v2, v2, v2
	v_max_f32_e32 v2, v2, v36
	v_add_f32_e32 v36, 0x7149f2ca, v2
	v_mul_f32_e32 v36, 0x3db504f3, v36
	v_cmp_ge_f32_e32 vcc, s42, v36
	s_cmp_eq_u64 vcc, exec
	s_cselect_b64 s[0:1], -1, 0
	s_andn2_b64 vcc, exec, s[34:35]
	s_cbranch_vccnz .LBB3_16
	s_waitcnt vmcnt(0)
	s_waitcnt vmcnt(3)
	ds_write_b128 v212, v[182:185] offset:16384
	s_waitcnt vmcnt(2)
	ds_write_b128 v213, v[178:181] offset:16384
	s_waitcnt vmcnt(1)
	ds_write_b128 v214, v[186:189] offset:49152
	s_waitcnt vmcnt(0)
	ds_write_b128 v214, v[190:193] offset:57344
	s_cmp_lt_u32 s59, s58
	s_cbranch_scc0 .Lwo_np_a
	v_cvt_pk_f16_f32 v246, v246, v247
	v_cvt_pk_f16_f32 v247, v248, v249
	v_cvt_pk_f16_f32 v248, v250, v251
	v_cvt_pk_f16_f32 v249, v252, v253
	s_lshl_b32 s61, s59, 13
	s_add_u32 s62, s56, s61
	s_addc_u32 s63, s57, 0
	global_store_dwordx4 v255, v[246:249], s[62:63]
	s_add_i32 s59, s59, 1

.LBB3_21:
	ds_read_b64_tr_b16 v[118:119], v207 offset:0
	ds_read_b64_tr_b16 v[120:121], v207 offset:0x800
	ds_read_b64_tr_b16 v[122:123], v207 offset:0x1000
	ds_read_b64_tr_b16 v[124:125], v207 offset:0x1800
	ds_read_b64_tr_b16 v[126:127], v207 offset:0x2000
	ds_read_b64_tr_b16 v[128:129], v207 offset:0x2800
	ds_read_b64_tr_b16 v[130:131], v207 offset:0x3000
	ds_read_b64_tr_b16 v[132:133], v207 offset:0x3800
	s_waitcnt lgkmcnt(0)
	s_nop 0
	v_mfma_f32_32x32x16_f16 v[66:81], v[118:121], v[4:7], v[66:81]
	v_max_f32_e32 v2, v99, v99
	v_max_f32_e32 v118, v98, v98
	v_max_f32_e32 v2, v118, v2
	v_max3_f32 v2, v2, v100, v101
	v_max3_f32 v2, v2, v102, v103
	v_max3_f32 v2, v2, v104, v105
	v_max3_f32 v2, v2, v106, v107
	v_mfma_f32_32x32x16_f16 v[66:81], v[122:125], v[8:11], v[66:81]
	v_max3_f32 v2, v2, v108, v109
	v_max3_f32 v2, v2, v110, v111
	v_max3_f32 v2, v2, v112, v113
	v_mfma_f32_32x32x16_f16 v[66:81], v[126:129], v[12:15], v[66:81]
	v_mfma_f32_32x32x16_f16 v[66:81], v[130:133], v[114:117], v[66:81]
	ds_read_b64_tr_b16 v[118:119], v207 offset:0x200
	ds_read_b64_tr_b16 v[120:121], v207 offset:0xa00
	ds_read_b64_tr_b16 v[122:123], v207 offset:0x1200
	ds_read_b64_tr_b16 v[124:125], v207 offset:0x1a00
	ds_read_b64_tr_b16 v[126:127], v207 offset:0x2200
	ds_read_b64_tr_b16 v[128:129], v207 offset:0x2a00
	ds_read_b64_tr_b16 v[130:131], v207 offset:0x3200
	ds_read_b64_tr_b16 v[132:133], v207 offset:0x3a00
	s_waitcnt lgkmcnt(0)
	s_nop 0
	v_mfma_f32_32x32x16_f16 v[50:65], v[118:121], v[4:7], v[50:65]
	v_max3_f32 v2, v2, v82, v83
	v_max3_f32 v2, v2, v84, v85
	v_max3_f32 v2, v2, v86, v87
	v_max3_f32 v2, v2, v88, v89
	v_max3_f32 v2, v2, v90, v91
	v_max3_f32 v2, v2, v92, v93
	v_max3_f32 v2, v2, v94, v95
	v_mfma_f32_32x32x16_f16 v[50:65], v[122:125], v[8:11], v[50:65]
	v_max3_f32 v2, v2, v96, v97
	v_mov_b32_e32 v118, v2
	s_nop 1
	v_permlane32_swap_b32_e32 v2, v118
	v_max_f32_e32 v118, v118, v118
	v_max_f32_e32 v2, v2, v2
	v_max_f32_e32 v2, v2, v118
	v_mfma_f32_32x32x16_f16 v[50:65], v[126:129], v[12:15], v[50:65]
	v_mfma_f32_32x32x16_f16 v[50:65], v[130:133], v[114:117], v[50:65]
	ds_read_b64_tr_b16 v[118:119], v207 offset:0x400
	ds_read_b64_tr_b16 v[120:121], v207 offset:0xc00
	ds_read_b64_tr_b16 v[122:123], v207 offset:0x1400
	ds_read_b64_tr_b16 v[124:125], v207 offset:0x1c00
	ds_read_b64_tr_b16 v[126:127], v207 offset:0x2400
	ds_read_b64_tr_b16 v[128:129], v207 offset:0x2c00
	ds_read_b64_tr_b16 v[130:131], v207 offset:0x3400
	ds_read_b64_tr_b16 v[132:133], v207 offset:0x3c00
	s_waitcnt lgkmcnt(0)
	s_nop 0
	v_mfma_f32_32x32x16_f16 v[34:49], v[118:121], v[4:7], v[34:49]
	v_sub_f32_e32 v118, v2, v194
	v_mul_f32_e32 v118, 0x3db504f3, v118
	v_cmp_ge_f32_e32 vcc, s42, v118
	s_cmp_eq_u64 vcc, exec
	v_max_f32_e32 v118, v194, v194
	v_max_f32_e32 v2, v118, v2
	s_cselect_b64 vcc, -1, 0
	v_mfma_f32_32x32x16_f16 v[34:49], v[122:125], v[8:11], v[34:49]
	v_cndmask_b32_e32 v226, v2, v194, vcc
	v_sub_f32_e32 v2, v194, v226
	v_mul_f32_e32 v2, 0x3e0293ee, v2
	v_exp_f32_e32 v2, v2
	s_nop 0
	v_cndmask_b32_e64 v2, v2, 1.0, vcc
	v_mfma_f32_32x32x16_f16 v[34:49], v[126:129], v[12:15], v[34:49]
	v_mfma_f32_32x32x16_f16 v[34:49], v[130:133], v[114:117], v[34:49]
	ds_read_b64_tr_b16 v[118:119], v207 offset:0x600
	ds_read_b64_tr_b16 v[120:121], v207 offset:0xe00
	ds_read_b64_tr_b16 v[122:123], v207 offset:0x1600
	ds_read_b64_tr_b16 v[124:125], v207 offset:0x1e00
	ds_read_b64_tr_b16 v[126:127], v207 offset:0x2600
	ds_read_b64_tr_b16 v[128:129], v207 offset:0x2e00
	ds_read_b64_tr_b16 v[130:131], v207 offset:0x3600
	ds_read_b64_tr_b16 v[132:133], v207 offset:0x3e00
	s_waitcnt lgkmcnt(0)
	s_nop 0
	v_mfma_f32_32x32x16_f16 v[18:33], v[118:121], v[4:7], v[18:33]
	v_mfma_f32_32x32x16_f16 v[18:33], v[122:125], v[8:11], v[18:33]
	v_mfma_f32_32x32x16_f16 v[18:33], v[126:129], v[12:15], v[18:33]
	v_mfma_f32_32x32x16_f16 v[18:33], v[130:133], v[114:117], v[18:33]
	s_barrier
	s_waitcnt vmcnt(0)
	v_cmp_gt_f32_e32 vcc, 1.0, v2
	s_waitcnt vmcnt(3)
	ds_write_b128 v212, v[182:185]
	s_waitcnt vmcnt(2)
	ds_write_b128 v213, v[178:181]
	s_waitcnt vmcnt(1)
	ds_write_b128 v214, v[186:189] offset:32768
	s_waitcnt vmcnt(0)
	ds_write_b128 v214, v[190:193] offset:40960
	s_cmp_lt_u32 s59, s58
	s_cbranch_scc0 .Lwo_np_b
	v_cvt_pk_f16_f32 v246, v246, v247
	v_cvt_pk_f16_f32 v247, v248, v249
	v_cvt_pk_f16_f32 v248, v250, v251
	v_cvt_pk_f16_f32 v249, v252, v253
	s_lshl_b32 s61, s59, 13
	s_add_u32 s62, s56, s61
	s_addc_u32 s63, s57, 0
	global_store_dwordx4 v255, v[246:249], s[62:63]
	s_add_i32 s59, s59, 1

.Lwo_tail:
	s_cmp_lt_u32 s59, s58
	s_cbranch_scc0 .Lwo_np_t
	s_waitcnt vmcnt(0)
	v_cvt_pk_f16_f32 v246, v246, v247
	v_cvt_pk_f16_f32 v247, v248, v249
	v_cvt_pk_f16_f32 v248, v250, v251
	v_cvt_pk_f16_f32 v249, v252, v253
	s_lshl_b32 s61, s59, 13
	s_add_u32 s62, s56, s61
	s_addc_u32 s63, s57, 0
	global_store_dwordx4 v255, v[246:249], s[62:63]
	s_add_i32 s59, s59, 1

amdhsa.kernels:
  - .agpr_count:     0
    .args:
      - .actual_access:  read_only
        .address_space:  global
        .offset:         0
        .size:           8
        .value_kind:     global_buffer
      - .actual_access:  read_only
        .address_space:  global
        .offset:         8
        .size:           8
        .value_kind:     global_buffer
      - .actual_access:  read_only
        .address_space:  global
        .offset:         16
        .size:           8
        .value_kind:     global_buffer
      - .actual_access:  read_only
        .address_space:  global
        .offset:         24
        .size:           8
        .value_kind:     global_buffer
      - .actual_access:  read_only
        .address_space:  global
        .offset:         32
        .size:           8
        .value_kind:     global_buffer
      - .address_space:  global
        .offset:         40
        .size:           8
        .value_kind:     global_buffer
      - .address_space:  global
        .offset:         48
        .size:           8
        .value_kind:     global_buffer
      - .address_space:  global
        .offset:         56
        .size:           8
        .value_kind:     global_buffer
      - .actual_access:  write_only
        .address_space:  global
        .offset:         64
        .size:           8
        .value_kind:     global_buffer
    .group_segment_fixed_size: 0
    .kernarg_segment_align: 8
    .kernarg_segment_size: 72
    .language:       OpenCL C
    .language_version:
      - 2
      - 0
    .max_flat_workgroup_size: 256
    .name:           _Z10cvt_kernelPKfS0_S0_S0_S0_PDF16_S1_S1_P15HIP_vector_typeIfLj2EE
    .private_segment_fixed_size: 0
    .sgpr_count:     30
    .sgpr_spill_count: 0
    .symbol:         _Z10cvt_kernelPKfS0_S0_S0_S0_PDF16_S1_S1_P15HIP_vector_typeIfLj2EE.kd
    .uniform_work_group_size: 1
    .uses_dynamic_stack: false
    .vgpr_count:     21
    .vgpr_spill_count: 0
    .wavefront_size: 64
  - .agpr_count:     0
    .args:
      - .address_space:  global
        .offset:         0
        .size:           8
        .value_kind:     global_buffer
      - .address_space:  global
        .offset:         8
        .size:           8
        .value_kind:     global_buffer
      - .address_space:  global
        .offset:         16
        .size:           8
        .value_kind:     global_buffer
      - .offset:         24
        .size:           4
        .value_kind:     by_value
      - .offset:         28
        .size:           4
        .value_kind:     by_value
      - .offset:         32
        .size:           4
        .value_kind:     by_value
    .group_segment_fixed_size: 0
    .kernarg_segment_align: 8
    .kernarg_segment_size: 36
    .language:       OpenCL C
    .language_version:
      - 2
      - 0
    .max_flat_workgroup_size: 512
    .name:           _Z15gemm_out_kernelPKDF16_S0_Pfiii
    .private_segment_fixed_size: 0
    .sgpr_count:     42
    .sgpr_spill_count: 0
    .symbol:         _Z15gemm_out_kernelPKDF16_S0_Pfiii.kd
    .uniform_work_group_size: 1
    .uses_dynamic_stack: false
    .vgpr_count:     247
    .vgpr_spill_count: 0
    .wavefront_size: 64
  - .agpr_count:     0
    .args:
      - .address_space:  global
        .offset:         0
        .size:           8
        .value_kind:     global_buffer
      - .address_space:  global
        .offset:         8
        .size:           8
        .value_kind:     global_buffer
      - .address_space:  global
        .offset:         16
        .size:           8
        .value_kind:     global_buffer
      - .actual_access:  read_only
        .address_space:  global
        .offset:         24
        .size:           8
        .value_kind:     global_buffer
      - .actual_access:  read_only
        .address_space:  global
        .offset:         32
        .size:           8
        .value_kind:     global_buffer
      - .actual_access:  read_only
        .address_space:  global
        .offset:         40
        .size:           8
        .value_kind:     global_buffer
    .group_segment_fixed_size: 0
    .kernarg_segment_align: 8
    .kernarg_segment_size: 48
    .language:       OpenCL C
    .language_version:
      - 2
      - 0
    .max_flat_workgroup_size: 512
    .name:           _Z15gemm_qkv_kernelPKDF16_S0_PDF16_PKfS3_PK15HIP_vector_typeIfLj2EE
    .private_segment_fixed_size: 0
    .sgpr_count:     64
    .sgpr_spill_count: 0
    .symbol:         _Z15gemm_qkv_kernelPKDF16_S0_PDF16_PKfS3_PK15HIP_vector_typeIfLj2EE.kd
    .uniform_work_group_size: 1
    .uses_dynamic_stack: false
    .vgpr_count:     236
    .vgpr_spill_count: 0
    .wavefront_size: 64
  - .agpr_count:     0
    .args:
      - .actual_access:  read_only
        .address_space:  global
        .offset:         0
        .size:           8
        .value_kind:     global_buffer
      - .actual_access:  write_only
        .address_space:  global
        .offset:         8
        .size:           8
        .value_kind:     global_buffer
      - .offset:         16
        .size:           4
        .value_kind:     hidden_block_count_x
      - .offset:         20
        .size:           4
        .value_kind:     hidden_block_count_y
      - .offset:         24
        .size:           4
        .value_kind:     hidden_block_count_z
      - .offset:         28
        .size:           2
        .value_kind:     hidden_group_size_x
      - .offset:         30
        .size:           2
        .value_kind:     hidden_group_size_y
      - .offset:         32
        .size:           2
        .value_kind:     hidden_group_size_z
      - .offset:         34
        .size:           2
        .value_kind:     hidden_remainder_x
      - .offset:         36
        .size:           2
        .value_kind:     hidden_remainder_y
      - .offset:         38
        .size:           2
        .value_kind:     hidden_remainder_z
      - .offset:         56
        .size:           8
        .value_kind:     hidden_global_offset_x
      - .offset:         64
        .size:           8
        .value_kind:     hidden_global_offset_y
      - .offset:         72
        .size:           8
        .value_kind:     hidden_global_offset_z
      - .offset:         80
        .size:           2
        .value_kind:     hidden_grid_dims
      - .offset:         136
        .size:           4
        .value_kind:     hidden_dynamic_lds_size
    .group_segment_fixed_size: 0
    .kernarg_segment_align: 8
    .kernarg_segment_size: 272
    .language:       OpenCL C
    .language_version:
      - 2
      - 0
    .max_flat_workgroup_size: 512
    .name:           _Z11attn_kernelPKDF16_PDF16_
    .private_segment_fixed_size: 0
    .sgpr_count:     70
    .sgpr_spill_count: 0
    .symbol:         _Z11attn_kernelPKDF16_PDF16_.kd
    .uniform_work_group_size: 1
    .uses_dynamic_stack: false
    .vgpr_count:     256
    .vgpr_spill_count: 0
    .wavefront_size: 64
